# row-scale loads of the S1 and FFN1 epilogues issued at the unit head (spare VGPRs), epilogue waits vmcnt(8) instead of vmcnt(0)
# baseline (speedup 1.0000x reference)
.LBB0_573:
	s_andn2_b64 vcc, exec, s[16:17]
	s_waitcnt vmcnt(0)
	v_lshl_add_u32 v248, s70, 8, v154
	v_ashrrev_i32_e32 v249, 31, v248
	v_lshl_add_u64 v[250:251], v[248:249], 2, s[14:15]
	global_load_dword v240, v[250:251], off
	global_load_dword v241, v[250:251], off offset:64
	global_load_dword v242, v[250:251], off offset:128
	global_load_dword v243, v[250:251], off offset:192
	global_load_dword v244, v[250:251], off offset:512
	global_load_dword v245, v[250:251], off offset:576
	global_load_dword v246, v[250:251], off offset:640
	global_load_dword v247, v[250:251], off offset:704
	s_cbranch_vccnz .LBB0_576
	s_add_u32 s71, s22, s40
	s_addc_u32 s72, s23, 0
	s_add_u32 s73, s0, s10
	s_addc_u32 s74, s1, s11
	s_add_u32 s75, s20, s10
	s_addc_u32 s76, s21, s11
	s_mov_b32 s77, 0
	v_mov_b32_e32 v2, 0
	v_mov_b32_e32 v3, 0
	v_mov_b32_e32 v4, 0
	v_mov_b32_e32 v5, 0
	s_nop 1
	v_mfma_f32_32x32x16_bf16 v[18:33], v[2:5], v[2:5], 0
	v_mfma_f32_32x32x16_bf16 v[34:49], v[2:5], v[2:5], 0
	v_mfma_f32_32x32x16_bf16 v[50:65], v[2:5], v[2:5], 0
	v_mfma_f32_32x32x16_bf16 v[66:81], v[2:5], v[2:5], 0
	v_mfma_f32_32x32x16_bf16 v[82:97], v[2:5], v[2:5], 0
	v_mfma_f32_32x32x16_bf16 v[98:113], v[2:5], v[2:5], 0
	v_mfma_f32_32x32x16_bf16 v[114:129], v[2:5], v[2:5], 0
	v_mfma_f32_16x16x32_bf16 v[6:9], v[2:5], v[2:5], 0
	v_mfma_f32_16x16x32_bf16 v[10:13], v[2:5], v[2:5], 0
	v_mfma_f32_16x16x32_bf16 v[14:17], v[2:5], v[2:5], 0

.Lpj_cm:
	s_mov_b32 s25, 0
	s_add_u32 s24, s34, s24
	s_addc_u32 s25, s35, s25
	v_readfirstlane_b32 s28, v156
	s_nop 3
	s_bfe_u32 s28, s28, 0x20005
	s_cmp_ge_u32 s28, 2
	s_cselect_b32 s23, s26, s23
	v_and_b32_e32 v172, -9, v154
	v_lshl_add_u32 v172, s70, 8, v172
	v_lshrrev_b32_e32 v174, 5, v156
	v_lshlrev_b32_e32 v174, 6, v174
	v_and_b32_e32 v144, 24, v156
	v_add_u32_e32 v174, v174, v144
	v_and_b32_e32 v144, 8, v154
	v_lshl_add_u32 v174, v144, 2, v174
	v_add_u32_e32 v174, s30, v174
	v_lshlrev_b32_e32 v174, 1, v174
	v_mov_b32_e32 v175, 0
	v_lshl_add_u64 v[176:177], s[24:25], 0, v[174:175]
	v_mad_u64_u32 v[178:179], vcc, v172, s22, v[176:177]
	v_mov_b32_e32 v184, 1.0
	v_mov_b32_e32 v185, 1.0
	v_mov_b32_e32 v186, 0xbfb8aa3b
	v_mov_b32_e32 v187, 0xbfb8aa3b
	v_mov_b32_e32 v188, 0x3d372713
	v_mov_b32_e32 v189, 0x3d372713
	v_mov_b32_e32 v190, 0x3fcc422a
	v_mov_b32_e32 v191, 0x3fcc422a
	s_mov_b32 s29, 0
	s_waitcnt vmcnt(8)
	s_cmp_eq_u32 s23, 1
	s_cbranch_scc1 .Lpj_gelu
	s_cmp_eq_u32 s23, 2
	s_cbranch_scc1 .Lpj_sigm
	v_pk_mul_f32 v[126:127], v[126:127], v[240:241] op_sel_hi:[1,0]
	v_pk_mul_f32 v[128:129], v[128:129], v[240:241] op_sel_hi:[1,0]
	v_pk_mul_f32 v[122:123], v[122:123], v[240:241] op_sel_hi:[1,0]
	v_pk_mul_f32 v[124:125], v[124:125], v[240:241] op_sel_hi:[1,0]
	v_cvt_pk_bf16_f32 v126, v126, v127
	v_cvt_pk_bf16_f32 v127, v128, v129
	v_cvt_pk_bf16_f32 v128, v122, v123
	v_cvt_pk_bf16_f32 v129, v124, v125
	v_pk_mul_f32 v[118:119], v[118:119], v[240:241] op_sel_hi:[1,0]
	v_pk_mul_f32 v[120:121], v[120:121], v[240:241] op_sel_hi:[1,0]
	v_pk_mul_f32 v[114:115], v[114:115], v[240:241] op_sel_hi:[1,0]
	v_pk_mul_f32 v[116:117], v[116:117], v[240:241] op_sel_hi:[1,0]
	v_cvt_pk_bf16_f32 v118, v118, v119
	v_cvt_pk_bf16_f32 v119, v120, v121
	v_cvt_pk_bf16_f32 v120, v114, v115
	v_cvt_pk_bf16_f32 v121, v116, v117
	v_mov_b32_e32 v158, v118
	v_mov_b32_e32 v159, v119
	v_mov_b32_e32 v160, v120
	v_mov_b32_e32 v161, v121
	v_mov_b32_dpp v118, v126 row_shl:8 row_mask:0xf bank_mask:0x3
	v_mov_b32_dpp v119, v127 row_shl:8 row_mask:0xf bank_mask:0x3
	v_mov_b32_dpp v120, v128 row_shl:8 row_mask:0xf bank_mask:0x3
	v_mov_b32_dpp v121, v129 row_shl:8 row_mask:0xf bank_mask:0x3
	v_mov_b32_dpp v126, v158 row_shr:8 row_mask:0xf bank_mask:0xc
	v_mov_b32_dpp v127, v159 row_shr:8 row_mask:0xf bank_mask:0xc
	v_mov_b32_dpp v128, v160 row_shr:8 row_mask:0xf bank_mask:0xc
	v_mov_b32_dpp v129, v161 row_shr:8 row_mask:0xf bank_mask:0xc
	s_mul_i32 s28, s22, 0
	v_lshl_add_u64 v[180:181], s[28:29], 0, v[178:179]
	global_store_dwordx4 v[180:181], v[126:129], off
	s_mul_i32 s28, s22, 8
	v_lshl_add_u64 v[180:181], s[28:29], 0, v[178:179]
	global_store_dwordx4 v[180:181], v[118:121], off
	v_pk_mul_f32 v[110:111], v[110:111], v[240:241] op_sel:[0,1] op_sel_hi:[1,1]
	v_pk_mul_f32 v[112:113], v[112:113], v[240:241] op_sel:[0,1] op_sel_hi:[1,1]
	v_pk_mul_f32 v[106:107], v[106:107], v[240:241] op_sel:[0,1] op_sel_hi:[1,1]
	v_pk_mul_f32 v[108:109], v[108:109], v[240:241] op_sel:[0,1] op_sel_hi:[1,1]
	v_cvt_pk_bf16_f32 v110, v110, v111
	v_cvt_pk_bf16_f32 v111, v112, v113
	v_cvt_pk_bf16_f32 v112, v106, v107
	v_cvt_pk_bf16_f32 v113, v108, v109
	v_pk_mul_f32 v[102:103], v[102:103], v[240:241] op_sel:[0,1] op_sel_hi:[1,1]
	v_pk_mul_f32 v[104:105], v[104:105], v[240:241] op_sel:[0,1] op_sel_hi:[1,1]
	v_pk_mul_f32 v[98:99], v[98:99], v[240:241] op_sel:[0,1] op_sel_hi:[1,1]
	v_pk_mul_f32 v[100:101], v[100:101], v[240:241] op_sel:[0,1] op_sel_hi:[1,1]
	v_cvt_pk_bf16_f32 v102, v102, v103
	v_cvt_pk_bf16_f32 v103, v104, v105
	v_cvt_pk_bf16_f32 v104, v98, v99
	v_cvt_pk_bf16_f32 v105, v100, v101
	v_mov_b32_e32 v158, v102
	v_mov_b32_e32 v159, v103
	v_mov_b32_e32 v160, v104
	v_mov_b32_e32 v161, v105
	v_mov_b32_dpp v102, v110 row_shl:8 row_mask:0xf bank_mask:0x3
	v_mov_b32_dpp v103, v111 row_shl:8 row_mask:0xf bank_mask:0x3
	v_mov_b32_dpp v104, v112 row_shl:8 row_mask:0xf bank_mask:0x3
	v_mov_b32_dpp v105, v113 row_shl:8 row_mask:0xf bank_mask:0x3
	v_mov_b32_dpp v110, v158 row_shr:8 row_mask:0xf bank_mask:0xc
	v_mov_b32_dpp v111, v159 row_shr:8 row_mask:0xf bank_mask:0xc
	v_mov_b32_dpp v112, v160 row_shr:8 row_mask:0xf bank_mask:0xc
	v_mov_b32_dpp v113, v161 row_shr:8 row_mask:0xf bank_mask:0xc
	s_mul_i32 s28, s22, 16
	v_lshl_add_u64 v[180:181], s[28:29], 0, v[178:179]
	global_store_dwordx4 v[180:181], v[110:113], off
	s_mul_i32 s28, s22, 24
	v_lshl_add_u64 v[180:181], s[28:29], 0, v[178:179]
	global_store_dwordx4 v[180:181], v[102:105], off
	v_pk_mul_f32 v[94:95], v[94:95], v[242:243] op_sel_hi:[1,0]
	v_pk_mul_f32 v[96:97], v[96:97], v[242:243] op_sel_hi:[1,0]
	v_pk_mul_f32 v[90:91], v[90:91], v[242:243] op_sel_hi:[1,0]
	v_pk_mul_f32 v[92:93], v[92:93], v[242:243] op_sel_hi:[1,0]
	v_cvt_pk_bf16_f32 v94, v94, v95
	v_cvt_pk_bf16_f32 v95, v96, v97
	v_cvt_pk_bf16_f32 v96, v90, v91
	v_cvt_pk_bf16_f32 v97, v92, v93
	v_pk_mul_f32 v[86:87], v[86:87], v[242:243] op_sel_hi:[1,0]
	v_pk_mul_f32 v[88:89], v[88:89], v[242:243] op_sel_hi:[1,0]
	v_pk_mul_f32 v[82:83], v[82:83], v[242:243] op_sel_hi:[1,0]
	v_pk_mul_f32 v[84:85], v[84:85], v[242:243] op_sel_hi:[1,0]
	v_cvt_pk_bf16_f32 v86, v86, v87
	v_cvt_pk_bf16_f32 v87, v88, v89
	v_cvt_pk_bf16_f32 v88, v82, v83
	v_cvt_pk_bf16_f32 v89, v84, v85
	v_mov_b32_e32 v158, v86
	v_mov_b32_e32 v159, v87
	v_mov_b32_e32 v160, v88
	v_mov_b32_e32 v161, v89
	v_mov_b32_dpp v86, v94 row_shl:8 row_mask:0xf bank_mask:0x3
	v_mov_b32_dpp v87, v95 row_shl:8 row_mask:0xf bank_mask:0x3
	v_mov_b32_dpp v88, v96 row_shl:8 row_mask:0xf bank_mask:0x3
	v_mov_b32_dpp v89, v97 row_shl:8 row_mask:0xf bank_mask:0x3
	v_mov_b32_dpp v94, v158 row_shr:8 row_mask:0xf bank_mask:0xc
	v_mov_b32_dpp v95, v159 row_shr:8 row_mask:0xf bank_mask:0xc
	v_mov_b32_dpp v96, v160 row_shr:8 row_mask:0xf bank_mask:0xc
	v_mov_b32_dpp v97, v161 row_shr:8 row_mask:0xf bank_mask:0xc
	s_mul_i32 s28, s22, 32
	v_lshl_add_u64 v[180:181], s[28:29], 0, v[178:179]
	global_store_dwordx4 v[180:181], v[94:97], off
	s_mul_i32 s28, s22, 40
	v_lshl_add_u64 v[180:181], s[28:29], 0, v[178:179]
	global_store_dwordx4 v[180:181], v[86:89], off
	v_pk_mul_f32 v[78:79], v[78:79], v[242:243] op_sel:[0,1] op_sel_hi:[1,1]
	v_pk_mul_f32 v[80:81], v[80:81], v[242:243] op_sel:[0,1] op_sel_hi:[1,1]
	v_pk_mul_f32 v[74:75], v[74:75], v[242:243] op_sel:[0,1] op_sel_hi:[1,1]
	v_pk_mul_f32 v[76:77], v[76:77], v[242:243] op_sel:[0,1] op_sel_hi:[1,1]
	v_cvt_pk_bf16_f32 v78, v78, v79
	v_cvt_pk_bf16_f32 v79, v80, v81
	v_cvt_pk_bf16_f32 v80, v74, v75
	v_cvt_pk_bf16_f32 v81, v76, v77
	v_pk_mul_f32 v[70:71], v[70:71], v[242:243] op_sel:[0,1] op_sel_hi:[1,1]
	v_pk_mul_f32 v[72:73], v[72:73], v[242:243] op_sel:[0,1] op_sel_hi:[1,1]
	v_pk_mul_f32 v[66:67], v[66:67], v[242:243] op_sel:[0,1] op_sel_hi:[1,1]
	v_pk_mul_f32 v[68:69], v[68:69], v[242:243] op_sel:[0,1] op_sel_hi:[1,1]
	v_cvt_pk_bf16_f32 v70, v70, v71
	v_cvt_pk_bf16_f32 v71, v72, v73
	v_cvt_pk_bf16_f32 v72, v66, v67
	v_cvt_pk_bf16_f32 v73, v68, v69
	v_mov_b32_e32 v158, v70
	v_mov_b32_e32 v159, v71
	v_mov_b32_e32 v160, v72
	v_mov_b32_e32 v161, v73
	v_mov_b32_dpp v70, v78 row_shl:8 row_mask:0xf bank_mask:0x3
	v_mov_b32_dpp v71, v79 row_shl:8 row_mask:0xf bank_mask:0x3
	v_mov_b32_dpp v72, v80 row_shl:8 row_mask:0xf bank_mask:0x3
	v_mov_b32_dpp v73, v81 row_shl:8 row_mask:0xf bank_mask:0x3
	v_mov_b32_dpp v78, v158 row_shr:8 row_mask:0xf bank_mask:0xc
	v_mov_b32_dpp v79, v159 row_shr:8 row_mask:0xf bank_mask:0xc
	v_mov_b32_dpp v80, v160 row_shr:8 row_mask:0xf bank_mask:0xc
	v_mov_b32_dpp v81, v161 row_shr:8 row_mask:0xf bank_mask:0xc
	s_mul_i32 s28, s22, 48
	v_lshl_add_u64 v[180:181], s[28:29], 0, v[178:179]
	global_store_dwordx4 v[180:181], v[78:81], off
	s_mul_i32 s28, s22, 56
	v_lshl_add_u64 v[180:181], s[28:29], 0, v[178:179]
	global_store_dwordx4 v[180:181], v[70:73], off
	v_pk_mul_f32 v[62:63], v[62:63], v[244:245] op_sel_hi:[1,0]
	v_pk_mul_f32 v[64:65], v[64:65], v[244:245] op_sel_hi:[1,0]
	v_pk_mul_f32 v[58:59], v[58:59], v[244:245] op_sel_hi:[1,0]
	v_pk_mul_f32 v[60:61], v[60:61], v[244:245] op_sel_hi:[1,0]
	v_cvt_pk_bf16_f32 v62, v62, v63
	v_cvt_pk_bf16_f32 v63, v64, v65
	v_cvt_pk_bf16_f32 v64, v58, v59
	v_cvt_pk_bf16_f32 v65, v60, v61
	v_pk_mul_f32 v[54:55], v[54:55], v[244:245] op_sel_hi:[1,0]
	v_pk_mul_f32 v[56:57], v[56:57], v[244:245] op_sel_hi:[1,0]
	v_pk_mul_f32 v[50:51], v[50:51], v[244:245] op_sel_hi:[1,0]
	v_pk_mul_f32 v[52:53], v[52:53], v[244:245] op_sel_hi:[1,0]
	v_cvt_pk_bf16_f32 v54, v54, v55
	v_cvt_pk_bf16_f32 v55, v56, v57
	v_cvt_pk_bf16_f32 v56, v50, v51
	v_cvt_pk_bf16_f32 v57, v52, v53
	v_mov_b32_e32 v158, v54
	v_mov_b32_e32 v159, v55
	v_mov_b32_e32 v160, v56
	v_mov_b32_e32 v161, v57
	v_mov_b32_dpp v54, v62 row_shl:8 row_mask:0xf bank_mask:0x3
	v_mov_b32_dpp v55, v63 row_shl:8 row_mask:0xf bank_mask:0x3
	v_mov_b32_dpp v56, v64 row_shl:8 row_mask:0xf bank_mask:0x3
	v_mov_b32_dpp v57, v65 row_shl:8 row_mask:0xf bank_mask:0x3
	v_mov_b32_dpp v62, v158 row_shr:8 row_mask:0xf bank_mask:0xc
	v_mov_b32_dpp v63, v159 row_shr:8 row_mask:0xf bank_mask:0xc
	v_mov_b32_dpp v64, v160 row_shr:8 row_mask:0xf bank_mask:0xc
	v_mov_b32_dpp v65, v161 row_shr:8 row_mask:0xf bank_mask:0xc
	s_mul_i32 s28, s22, 128
	v_lshl_add_u64 v[180:181], s[28:29], 0, v[178:179]
	global_store_dwordx4 v[180:181], v[62:65], off
	s_mul_i32 s28, s22, 136
	v_lshl_add_u64 v[180:181], s[28:29], 0, v[178:179]
	global_store_dwordx4 v[180:181], v[54:57], off
	v_pk_mul_f32 v[46:47], v[46:47], v[244:245] op_sel:[0,1] op_sel_hi:[1,1]
	v_pk_mul_f32 v[48:49], v[48:49], v[244:245] op_sel:[0,1] op_sel_hi:[1,1]
	v_pk_mul_f32 v[42:43], v[42:43], v[244:245] op_sel:[0,1] op_sel_hi:[1,1]
	v_pk_mul_f32 v[44:45], v[44:45], v[244:245] op_sel:[0,1] op_sel_hi:[1,1]
	v_cvt_pk_bf16_f32 v46, v46, v47
	v_cvt_pk_bf16_f32 v47, v48, v49
	v_cvt_pk_bf16_f32 v48, v42, v43
	v_cvt_pk_bf16_f32 v49, v44, v45
	v_pk_mul_f32 v[38:39], v[38:39], v[244:245] op_sel:[0,1] op_sel_hi:[1,1]
	v_pk_mul_f32 v[40:41], v[40:41], v[244:245] op_sel:[0,1] op_sel_hi:[1,1]
	v_pk_mul_f32 v[34:35], v[34:35], v[244:245] op_sel:[0,1] op_sel_hi:[1,1]
	v_pk_mul_f32 v[36:37], v[36:37], v[244:245] op_sel:[0,1] op_sel_hi:[1,1]
	v_cvt_pk_bf16_f32 v38, v38, v39
	v_cvt_pk_bf16_f32 v39, v40, v41
	v_cvt_pk_bf16_f32 v40, v34, v35
	v_cvt_pk_bf16_f32 v41, v36, v37
	v_mov_b32_e32 v158, v38
	v_mov_b32_e32 v159, v39
	v_mov_b32_e32 v160, v40
	v_mov_b32_e32 v161, v41
	v_mov_b32_dpp v38, v46 row_shl:8 row_mask:0xf bank_mask:0x3
	v_mov_b32_dpp v39, v47 row_shl:8 row_mask:0xf bank_mask:0x3
	v_mov_b32_dpp v40, v48 row_shl:8 row_mask:0xf bank_mask:0x3
	v_mov_b32_dpp v41, v49 row_shl:8 row_mask:0xf bank_mask:0x3
	v_mov_b32_dpp v46, v158 row_shr:8 row_mask:0xf bank_mask:0xc
	v_mov_b32_dpp v47, v159 row_shr:8 row_mask:0xf bank_mask:0xc
	v_mov_b32_dpp v48, v160 row_shr:8 row_mask:0xf bank_mask:0xc
	v_mov_b32_dpp v49, v161 row_shr:8 row_mask:0xf bank_mask:0xc
	s_mul_i32 s28, s22, 144
	v_lshl_add_u64 v[180:181], s[28:29], 0, v[178:179]
	global_store_dwordx4 v[180:181], v[46:49], off
	s_mul_i32 s28, s22, 152
	v_lshl_add_u64 v[180:181], s[28:29], 0, v[178:179]
	global_store_dwordx4 v[180:181], v[38:41], off
	v_pk_mul_f32 v[30:31], v[30:31], v[246:247] op_sel_hi:[1,0]
	v_pk_mul_f32 v[32:33], v[32:33], v[246:247] op_sel_hi:[1,0]
	v_pk_mul_f32 v[26:27], v[26:27], v[246:247] op_sel_hi:[1,0]
	v_pk_mul_f32 v[28:29], v[28:29], v[246:247] op_sel_hi:[1,0]
	v_cvt_pk_bf16_f32 v30, v30, v31
	v_cvt_pk_bf16_f32 v31, v32, v33
	v_cvt_pk_bf16_f32 v32, v26, v27
	v_cvt_pk_bf16_f32 v33, v28, v29
	v_pk_mul_f32 v[22:23], v[22:23], v[246:247] op_sel_hi:[1,0]
	v_pk_mul_f32 v[24:25], v[24:25], v[246:247] op_sel_hi:[1,0]
	v_pk_mul_f32 v[18:19], v[18:19], v[246:247] op_sel_hi:[1,0]
	v_pk_mul_f32 v[20:21], v[20:21], v[246:247] op_sel_hi:[1,0]
	v_cvt_pk_bf16_f32 v22, v22, v23
	v_cvt_pk_bf16_f32 v23, v24, v25
	v_cvt_pk_bf16_f32 v24, v18, v19
	v_cvt_pk_bf16_f32 v25, v20, v21
	v_mov_b32_e32 v158, v22
	v_mov_b32_e32 v159, v23
	v_mov_b32_e32 v160, v24
	v_mov_b32_e32 v161, v25
	v_mov_b32_dpp v22, v30 row_shl:8 row_mask:0xf bank_mask:0x3
	v_mov_b32_dpp v23, v31 row_shl:8 row_mask:0xf bank_mask:0x3
	v_mov_b32_dpp v24, v32 row_shl:8 row_mask:0xf bank_mask:0x3
	v_mov_b32_dpp v25, v33 row_shl:8 row_mask:0xf bank_mask:0x3
	v_mov_b32_dpp v30, v158 row_shr:8 row_mask:0xf bank_mask:0xc
	v_mov_b32_dpp v31, v159 row_shr:8 row_mask:0xf bank_mask:0xc
	v_mov_b32_dpp v32, v160 row_shr:8 row_mask:0xf bank_mask:0xc
	v_mov_b32_dpp v33, v161 row_shr:8 row_mask:0xf bank_mask:0xc
	s_mul_i32 s28, s22, 160
	v_lshl_add_u64 v[180:181], s[28:29], 0, v[178:179]
	global_store_dwordx4 v[180:181], v[30:33], off
	s_mul_i32 s28, s22, 168
	v_lshl_add_u64 v[180:181], s[28:29], 0, v[178:179]
	global_store_dwordx4 v[180:181], v[22:25], off
	v_pk_mul_f32 v[14:15], v[14:15], v[246:247] op_sel:[0,1] op_sel_hi:[1,1]
	v_pk_mul_f32 v[16:17], v[16:17], v[246:247] op_sel:[0,1] op_sel_hi:[1,1]
	v_pk_mul_f32 v[10:11], v[10:11], v[246:247] op_sel:[0,1] op_sel_hi:[1,1]
	v_pk_mul_f32 v[12:13], v[12:13], v[246:247] op_sel:[0,1] op_sel_hi:[1,1]
	v_cvt_pk_bf16_f32 v14, v14, v15
	v_cvt_pk_bf16_f32 v15, v16, v17
	v_cvt_pk_bf16_f32 v16, v10, v11
	v_cvt_pk_bf16_f32 v17, v12, v13
	v_pk_mul_f32 v[6:7], v[6:7], v[246:247] op_sel:[0,1] op_sel_hi:[1,1]
	v_pk_mul_f32 v[8:9], v[8:9], v[246:247] op_sel:[0,1] op_sel_hi:[1,1]
	v_pk_mul_f32 v[2:3], v[2:3], v[246:247] op_sel:[0,1] op_sel_hi:[1,1]
	v_pk_mul_f32 v[4:5], v[4:5], v[246:247] op_sel:[0,1] op_sel_hi:[1,1]
	v_cvt_pk_bf16_f32 v6, v6, v7
	v_cvt_pk_bf16_f32 v7, v8, v9
	v_cvt_pk_bf16_f32 v8, v2, v3
	v_cvt_pk_bf16_f32 v9, v4, v5
	v_mov_b32_e32 v158, v6
	v_mov_b32_e32 v159, v7
	v_mov_b32_e32 v160, v8
	v_mov_b32_e32 v161, v9
	v_mov_b32_dpp v6, v14 row_shl:8 row_mask:0xf bank_mask:0x3
	v_mov_b32_dpp v7, v15 row_shl:8 row_mask:0xf bank_mask:0x3
	v_mov_b32_dpp v8, v16 row_shl:8 row_mask:0xf bank_mask:0x3
	v_mov_b32_dpp v9, v17 row_shl:8 row_mask:0xf bank_mask:0x3
	v_mov_b32_dpp v14, v158 row_shr:8 row_mask:0xf bank_mask:0xc
	v_mov_b32_dpp v15, v159 row_shr:8 row_mask:0xf bank_mask:0xc
	v_mov_b32_dpp v16, v160 row_shr:8 row_mask:0xf bank_mask:0xc
	v_mov_b32_dpp v17, v161 row_shr:8 row_mask:0xf bank_mask:0xc
	s_mul_i32 s28, s22, 176
	v_lshl_add_u64 v[180:181], s[28:29], 0, v[178:179]
	global_store_dwordx4 v[180:181], v[14:17], off
	s_mul_i32 s28, s22, 184
	v_lshl_add_u64 v[180:181], s[28:29], 0, v[178:179]
	global_store_dwordx4 v[180:181], v[6:9], off
	s_branch .Lpj_done
.Lpj_gelu:
	v_pk_mul_f32 v[126:127], v[126:127], v[240:241] op_sel_hi:[1,0]
	v_pk_mul_f32 v[128:129], v[128:129], v[240:241] op_sel_hi:[1,0]
	v_pk_mul_f32 v[122:123], v[122:123], v[240:241] op_sel_hi:[1,0]
	v_pk_mul_f32 v[124:125], v[124:125], v[240:241] op_sel_hi:[1,0]
	v_pk_mul_f32 v[144:145], v[126:127], v[188:189]
	v_pk_mul_f32 v[146:147], v[128:129], v[188:189]
	v_pk_mul_f32 v[148:149], v[122:123], v[188:189]
	v_pk_mul_f32 v[150:151], v[124:125], v[188:189]
	v_pk_mul_f32 v[144:145], v[126:127], v[144:145]
	v_pk_mul_f32 v[146:147], v[128:129], v[146:147]
	v_pk_mul_f32 v[148:149], v[122:123], v[148:149]
	v_pk_mul_f32 v[150:151], v[124:125], v[150:151]
	v_pk_fma_f32 v[144:145], v[126:127], v[144:145], v[126:127]
	v_pk_fma_f32 v[146:147], v[128:129], v[146:147], v[128:129]
	v_pk_fma_f32 v[148:149], v[122:123], v[148:149], v[122:123]
	v_pk_fma_f32 v[150:151], v[124:125], v[150:151], v[124:125]
	v_pk_mul_f32 v[144:145], v[144:145], v[190:191]
	v_pk_mul_f32 v[146:147], v[146:147], v[190:191]
	v_pk_mul_f32 v[148:149], v[148:149], v[190:191]
	v_pk_mul_f32 v[150:151], v[150:151], v[190:191]
	v_pk_mul_f32 v[144:145], v[144:145], v[186:187]
	v_pk_mul_f32 v[146:147], v[146:147], v[186:187]
	v_pk_mul_f32 v[148:149], v[148:149], v[186:187]
	v_pk_mul_f32 v[150:151], v[150:151], v[186:187]
	v_exp_f32_e32 v144, v144
	v_exp_f32_e32 v145, v145
	v_exp_f32_e32 v146, v146
	v_exp_f32_e32 v147, v147
	v_exp_f32_e32 v148, v148
	v_exp_f32_e32 v149, v149
	v_exp_f32_e32 v150, v150
	v_exp_f32_e32 v151, v151
	s_nop 0
	v_pk_add_f32 v[144:145], v[144:145], v[184:185]
	v_pk_add_f32 v[146:147], v[146:147], v[184:185]
	v_pk_add_f32 v[148:149], v[148:149], v[184:185]
	v_pk_add_f32 v[150:151], v[150:151], v[184:185]
	v_rcp_f32_e32 v144, v144
	v_rcp_f32_e32 v145, v145
	v_rcp_f32_e32 v146, v146
	v_rcp_f32_e32 v147, v147
	v_rcp_f32_e32 v148, v148
	v_rcp_f32_e32 v149, v149
	v_rcp_f32_e32 v150, v150
	v_rcp_f32_e32 v151, v151
	s_nop 0
	v_pk_mul_f32 v[126:127], v[126:127], v[144:145]
	v_pk_mul_f32 v[128:129], v[128:129], v[146:147]
	v_pk_mul_f32 v[122:123], v[122:123], v[148:149]
	v_pk_mul_f32 v[124:125], v[124:125], v[150:151]
	v_cvt_pk_bf16_f32 v126, v126, v127
	v_cvt_pk_bf16_f32 v127, v128, v129
	v_cvt_pk_bf16_f32 v128, v122, v123
	v_cvt_pk_bf16_f32 v129, v124, v125
	v_pk_mul_f32 v[118:119], v[118:119], v[240:241] op_sel_hi:[1,0]
	v_pk_mul_f32 v[120:121], v[120:121], v[240:241] op_sel_hi:[1,0]
	v_pk_mul_f32 v[114:115], v[114:115], v[240:241] op_sel_hi:[1,0]
	v_pk_mul_f32 v[116:117], v[116:117], v[240:241] op_sel_hi:[1,0]
	v_pk_mul_f32 v[144:145], v[118:119], v[188:189]
	v_pk_mul_f32 v[146:147], v[120:121], v[188:189]
	v_pk_mul_f32 v[148:149], v[114:115], v[188:189]
	v_pk_mul_f32 v[150:151], v[116:117], v[188:189]
	v_pk_mul_f32 v[144:145], v[118:119], v[144:145]
	v_pk_mul_f32 v[146:147], v[120:121], v[146:147]
	v_pk_mul_f32 v[148:149], v[114:115], v[148:149]
	v_pk_mul_f32 v[150:151], v[116:117], v[150:151]
	v_pk_fma_f32 v[144:145], v[118:119], v[144:145], v[118:119]
	v_pk_fma_f32 v[146:147], v[120:121], v[146:147], v[120:121]
	v_pk_fma_f32 v[148:149], v[114:115], v[148:149], v[114:115]
	v_pk_fma_f32 v[150:151], v[116:117], v[150:151], v[116:117]
	v_pk_mul_f32 v[144:145], v[144:145], v[190:191]
	v_pk_mul_f32 v[146:147], v[146:147], v[190:191]
	v_pk_mul_f32 v[148:149], v[148:149], v[190:191]
	v_pk_mul_f32 v[150:151], v[150:151], v[190:191]
	v_pk_mul_f32 v[144:145], v[144:145], v[186:187]
	v_pk_mul_f32 v[146:147], v[146:147], v[186:187]
	v_pk_mul_f32 v[148:149], v[148:149], v[186:187]
	v_pk_mul_f32 v[150:151], v[150:151], v[186:187]
	v_exp_f32_e32 v144, v144
	v_exp_f32_e32 v145, v145
	v_exp_f32_e32 v146, v146
	v_exp_f32_e32 v147, v147
	v_exp_f32_e32 v148, v148
	v_exp_f32_e32 v149, v149
	v_exp_f32_e32 v150, v150
	v_exp_f32_e32 v151, v151
	s_nop 0
	v_pk_add_f32 v[144:145], v[144:145], v[184:185]
	v_pk_add_f32 v[146:147], v[146:147], v[184:185]
	v_pk_add_f32 v[148:149], v[148:149], v[184:185]
	v_pk_add_f32 v[150:151], v[150:151], v[184:185]
	v_rcp_f32_e32 v144, v144
	v_rcp_f32_e32 v145, v145
	v_rcp_f32_e32 v146, v146
	v_rcp_f32_e32 v147, v147
	v_rcp_f32_e32 v148, v148
	v_rcp_f32_e32 v149, v149
	v_rcp_f32_e32 v150, v150
	v_rcp_f32_e32 v151, v151
	s_nop 0
	v_pk_mul_f32 v[118:119], v[118:119], v[144:145]
	v_pk_mul_f32 v[120:121], v[120:121], v[146:147]
	v_pk_mul_f32 v[114:115], v[114:115], v[148:149]
	v_pk_mul_f32 v[116:117], v[116:117], v[150:151]
	v_cvt_pk_bf16_f32 v118, v118, v119
	v_cvt_pk_bf16_f32 v119, v120, v121
	v_cvt_pk_bf16_f32 v120, v114, v115
	v_cvt_pk_bf16_f32 v121, v116, v117
	v_mov_b32_e32 v158, v118
	v_mov_b32_e32 v159, v119
	v_mov_b32_e32 v160, v120
	v_mov_b32_e32 v161, v121
	v_mov_b32_dpp v118, v126 row_shl:8 row_mask:0xf bank_mask:0x3
	v_mov_b32_dpp v119, v127 row_shl:8 row_mask:0xf bank_mask:0x3
	v_mov_b32_dpp v120, v128 row_shl:8 row_mask:0xf bank_mask:0x3
	v_mov_b32_dpp v121, v129 row_shl:8 row_mask:0xf bank_mask:0x3
	v_mov_b32_dpp v126, v158 row_shr:8 row_mask:0xf bank_mask:0xc
	v_mov_b32_dpp v127, v159 row_shr:8 row_mask:0xf bank_mask:0xc
	v_mov_b32_dpp v128, v160 row_shr:8 row_mask:0xf bank_mask:0xc
	v_mov_b32_dpp v129, v161 row_shr:8 row_mask:0xf bank_mask:0xc
	s_mul_i32 s28, s22, 0
	v_lshl_add_u64 v[180:181], s[28:29], 0, v[178:179]
	global_store_dwordx4 v[180:181], v[126:129], off
	s_mul_i32 s28, s22, 8
	v_lshl_add_u64 v[180:181], s[28:29], 0, v[178:179]
	global_store_dwordx4 v[180:181], v[118:121], off
	v_pk_mul_f32 v[110:111], v[110:111], v[240:241] op_sel:[0,1] op_sel_hi:[1,1]
	v_pk_mul_f32 v[112:113], v[112:113], v[240:241] op_sel:[0,1] op_sel_hi:[1,1]
	v_pk_mul_f32 v[106:107], v[106:107], v[240:241] op_sel:[0,1] op_sel_hi:[1,1]
	v_pk_mul_f32 v[108:109], v[108:109], v[240:241] op_sel:[0,1] op_sel_hi:[1,1]
	v_pk_mul_f32 v[144:145], v[110:111], v[188:189]
	v_pk_mul_f32 v[146:147], v[112:113], v[188:189]
	v_pk_mul_f32 v[148:149], v[106:107], v[188:189]
	v_pk_mul_f32 v[150:151], v[108:109], v[188:189]
	v_pk_mul_f32 v[144:145], v[110:111], v[144:145]
	v_pk_mul_f32 v[146:147], v[112:113], v[146:147]
	v_pk_mul_f32 v[148:149], v[106:107], v[148:149]
	v_pk_mul_f32 v[150:151], v[108:109], v[150:151]
	v_pk_fma_f32 v[144:145], v[110:111], v[144:145], v[110:111]
	v_pk_fma_f32 v[146:147], v[112:113], v[146:147], v[112:113]
	v_pk_fma_f32 v[148:149], v[106:107], v[148:149], v[106:107]
	v_pk_fma_f32 v[150:151], v[108:109], v[150:151], v[108:109]
	v_pk_mul_f32 v[144:145], v[144:145], v[190:191]
	v_pk_mul_f32 v[146:147], v[146:147], v[190:191]
	v_pk_mul_f32 v[148:149], v[148:149], v[190:191]
	v_pk_mul_f32 v[150:151], v[150:151], v[190:191]
	v_pk_mul_f32 v[144:145], v[144:145], v[186:187]
	v_pk_mul_f32 v[146:147], v[146:147], v[186:187]
	v_pk_mul_f32 v[148:149], v[148:149], v[186:187]
	v_pk_mul_f32 v[150:151], v[150:151], v[186:187]
	v_exp_f32_e32 v144, v144
	v_exp_f32_e32 v145, v145
	v_exp_f32_e32 v146, v146
	v_exp_f32_e32 v147, v147
	v_exp_f32_e32 v148, v148
	v_exp_f32_e32 v149, v149
	v_exp_f32_e32 v150, v150
	v_exp_f32_e32 v151, v151
	s_nop 0
	v_pk_add_f32 v[144:145], v[144:145], v[184:185]
	v_pk_add_f32 v[146:147], v[146:147], v[184:185]
	v_pk_add_f32 v[148:149], v[148:149], v[184:185]
	v_pk_add_f32 v[150:151], v[150:151], v[184:185]
	v_rcp_f32_e32 v144, v144
	v_rcp_f32_e32 v145, v145
	v_rcp_f32_e32 v146, v146
	v_rcp_f32_e32 v147, v147
	v_rcp_f32_e32 v148, v148
	v_rcp_f32_e32 v149, v149
	v_rcp_f32_e32 v150, v150
	v_rcp_f32_e32 v151, v151
	s_nop 0
	v_pk_mul_f32 v[110:111], v[110:111], v[144:145]
	v_pk_mul_f32 v[112:113], v[112:113], v[146:147]
	v_pk_mul_f32 v[106:107], v[106:107], v[148:149]
	v_pk_mul_f32 v[108:109], v[108:109], v[150:151]
	v_cvt_pk_bf16_f32 v110, v110, v111
	v_cvt_pk_bf16_f32 v111, v112, v113
	v_cvt_pk_bf16_f32 v112, v106, v107
	v_cvt_pk_bf16_f32 v113, v108, v109
	v_pk_mul_f32 v[102:103], v[102:103], v[240:241] op_sel:[0,1] op_sel_hi:[1,1]
	v_pk_mul_f32 v[104:105], v[104:105], v[240:241] op_sel:[0,1] op_sel_hi:[1,1]
	v_pk_mul_f32 v[98:99], v[98:99], v[240:241] op_sel:[0,1] op_sel_hi:[1,1]
	v_pk_mul_f32 v[100:101], v[100:101], v[240:241] op_sel:[0,1] op_sel_hi:[1,1]
	v_pk_mul_f32 v[144:145], v[102:103], v[188:189]
	v_pk_mul_f32 v[146:147], v[104:105], v[188:189]
	v_pk_mul_f32 v[148:149], v[98:99], v[188:189]
	v_pk_mul_f32 v[150:151], v[100:101], v[188:189]
	v_pk_mul_f32 v[144:145], v[102:103], v[144:145]
	v_pk_mul_f32 v[146:147], v[104:105], v[146:147]
	v_pk_mul_f32 v[148:149], v[98:99], v[148:149]
	v_pk_mul_f32 v[150:151], v[100:101], v[150:151]
	v_pk_fma_f32 v[144:145], v[102:103], v[144:145], v[102:103]
	v_pk_fma_f32 v[146:147], v[104:105], v[146:147], v[104:105]
	v_pk_fma_f32 v[148:149], v[98:99], v[148:149], v[98:99]
	v_pk_fma_f32 v[150:151], v[100:101], v[150:151], v[100:101]
	v_pk_mul_f32 v[144:145], v[144:145], v[190:191]
	v_pk_mul_f32 v[146:147], v[146:147], v[190:191]
	v_pk_mul_f32 v[148:149], v[148:149], v[190:191]
	v_pk_mul_f32 v[150:151], v[150:151], v[190:191]
	v_pk_mul_f32 v[144:145], v[144:145], v[186:187]
	v_pk_mul_f32 v[146:147], v[146:147], v[186:187]
	v_pk_mul_f32 v[148:149], v[148:149], v[186:187]
	v_pk_mul_f32 v[150:151], v[150:151], v[186:187]
	v_exp_f32_e32 v144, v144
	v_exp_f32_e32 v145, v145
	v_exp_f32_e32 v146, v146
	v_exp_f32_e32 v147, v147
	v_exp_f32_e32 v148, v148
	v_exp_f32_e32 v149, v149
	v_exp_f32_e32 v150, v150
	v_exp_f32_e32 v151, v151
	s_nop 0
	v_pk_add_f32 v[144:145], v[144:145], v[184:185]
	v_pk_add_f32 v[146:147], v[146:147], v[184:185]
	v_pk_add_f32 v[148:149], v[148:149], v[184:185]
	v_pk_add_f32 v[150:151], v[150:151], v[184:185]
	v_rcp_f32_e32 v144, v144
	v_rcp_f32_e32 v145, v145
	v_rcp_f32_e32 v146, v146
	v_rcp_f32_e32 v147, v147
	v_rcp_f32_e32 v148, v148
	v_rcp_f32_e32 v149, v149
	v_rcp_f32_e32 v150, v150
	v_rcp_f32_e32 v151, v151
	s_nop 0
	v_pk_mul_f32 v[102:103], v[102:103], v[144:145]
	v_pk_mul_f32 v[104:105], v[104:105], v[146:147]
	v_pk_mul_f32 v[98:99], v[98:99], v[148:149]
	v_pk_mul_f32 v[100:101], v[100:101], v[150:151]
	v_cvt_pk_bf16_f32 v102, v102, v103
	v_cvt_pk_bf16_f32 v103, v104, v105
	v_cvt_pk_bf16_f32 v104, v98, v99
	v_cvt_pk_bf16_f32 v105, v100, v101
	v_mov_b32_e32 v158, v102
	v_mov_b32_e32 v159, v103
	v_mov_b32_e32 v160, v104
	v_mov_b32_e32 v161, v105
	v_mov_b32_dpp v102, v110 row_shl:8 row_mask:0xf bank_mask:0x3
	v_mov_b32_dpp v103, v111 row_shl:8 row_mask:0xf bank_mask:0x3
	v_mov_b32_dpp v104, v112 row_shl:8 row_mask:0xf bank_mask:0x3
	v_mov_b32_dpp v105, v113 row_shl:8 row_mask:0xf bank_mask:0x3
	v_mov_b32_dpp v110, v158 row_shr:8 row_mask:0xf bank_mask:0xc
	v_mov_b32_dpp v111, v159 row_shr:8 row_mask:0xf bank_mask:0xc
	v_mov_b32_dpp v112, v160 row_shr:8 row_mask:0xf bank_mask:0xc
	v_mov_b32_dpp v113, v161 row_shr:8 row_mask:0xf bank_mask:0xc
	s_mul_i32 s28, s22, 16
	v_lshl_add_u64 v[180:181], s[28:29], 0, v[178:179]
	global_store_dwordx4 v[180:181], v[110:113], off
	s_mul_i32 s28, s22, 24
	v_lshl_add_u64 v[180:181], s[28:29], 0, v[178:179]
	global_store_dwordx4 v[180:181], v[102:105], off
	v_pk_mul_f32 v[94:95], v[94:95], v[242:243] op_sel_hi:[1,0]
	v_pk_mul_f32 v[96:97], v[96:97], v[242:243] op_sel_hi:[1,0]
	v_pk_mul_f32 v[90:91], v[90:91], v[242:243] op_sel_hi:[1,0]
	v_pk_mul_f32 v[92:93], v[92:93], v[242:243] op_sel_hi:[1,0]
	v_pk_mul_f32 v[144:145], v[94:95], v[188:189]
	v_pk_mul_f32 v[146:147], v[96:97], v[188:189]
	v_pk_mul_f32 v[148:149], v[90:91], v[188:189]
	v_pk_mul_f32 v[150:151], v[92:93], v[188:189]
	v_pk_mul_f32 v[144:145], v[94:95], v[144:145]
	v_pk_mul_f32 v[146:147], v[96:97], v[146:147]
	v_pk_mul_f32 v[148:149], v[90:91], v[148:149]
	v_pk_mul_f32 v[150:151], v[92:93], v[150:151]
	v_pk_fma_f32 v[144:145], v[94:95], v[144:145], v[94:95]
	v_pk_fma_f32 v[146:147], v[96:97], v[146:147], v[96:97]
	v_pk_fma_f32 v[148:149], v[90:91], v[148:149], v[90:91]
	v_pk_fma_f32 v[150:151], v[92:93], v[150:151], v[92:93]
	v_pk_mul_f32 v[144:145], v[144:145], v[190:191]
	v_pk_mul_f32 v[146:147], v[146:147], v[190:191]
	v_pk_mul_f32 v[148:149], v[148:149], v[190:191]
	v_pk_mul_f32 v[150:151], v[150:151], v[190:191]
	v_pk_mul_f32 v[144:145], v[144:145], v[186:187]
	v_pk_mul_f32 v[146:147], v[146:147], v[186:187]
	v_pk_mul_f32 v[148:149], v[148:149], v[186:187]
	v_pk_mul_f32 v[150:151], v[150:151], v[186:187]
	v_exp_f32_e32 v144, v144
	v_exp_f32_e32 v145, v145
	v_exp_f32_e32 v146, v146
	v_exp_f32_e32 v147, v147
	v_exp_f32_e32 v148, v148
	v_exp_f32_e32 v149, v149
	v_exp_f32_e32 v150, v150
	v_exp_f32_e32 v151, v151
	s_nop 0
	v_pk_add_f32 v[144:145], v[144:145], v[184:185]
	v_pk_add_f32 v[146:147], v[146:147], v[184:185]
	v_pk_add_f32 v[148:149], v[148:149], v[184:185]
	v_pk_add_f32 v[150:151], v[150:151], v[184:185]
	v_rcp_f32_e32 v144, v144
	v_rcp_f32_e32 v145, v145
	v_rcp_f32_e32 v146, v146
	v_rcp_f32_e32 v147, v147
	v_rcp_f32_e32 v148, v148
	v_rcp_f32_e32 v149, v149
	v_rcp_f32_e32 v150, v150
	v_rcp_f32_e32 v151, v151
	s_nop 0
	v_pk_mul_f32 v[94:95], v[94:95], v[144:145]
	v_pk_mul_f32 v[96:97], v[96:97], v[146:147]
	v_pk_mul_f32 v[90:91], v[90:91], v[148:149]
	v_pk_mul_f32 v[92:93], v[92:93], v[150:151]
	v_cvt_pk_bf16_f32 v94, v94, v95
	v_cvt_pk_bf16_f32 v95, v96, v97
	v_cvt_pk_bf16_f32 v96, v90, v91
	v_cvt_pk_bf16_f32 v97, v92, v93
	v_pk_mul_f32 v[86:87], v[86:87], v[242:243] op_sel_hi:[1,0]
	v_pk_mul_f32 v[88:89], v[88:89], v[242:243] op_sel_hi:[1,0]
	v_pk_mul_f32 v[82:83], v[82:83], v[242:243] op_sel_hi:[1,0]
	v_pk_mul_f32 v[84:85], v[84:85], v[242:243] op_sel_hi:[1,0]
	v_pk_mul_f32 v[144:145], v[86:87], v[188:189]
	v_pk_mul_f32 v[146:147], v[88:89], v[188:189]
	v_pk_mul_f32 v[148:149], v[82:83], v[188:189]
	v_pk_mul_f32 v[150:151], v[84:85], v[188:189]
	v_pk_mul_f32 v[144:145], v[86:87], v[144:145]
	v_pk_mul_f32 v[146:147], v[88:89], v[146:147]
	v_pk_mul_f32 v[148:149], v[82:83], v[148:149]
	v_pk_mul_f32 v[150:151], v[84:85], v[150:151]
	v_pk_fma_f32 v[144:145], v[86:87], v[144:145], v[86:87]
	v_pk_fma_f32 v[146:147], v[88:89], v[146:147], v[88:89]
	v_pk_fma_f32 v[148:149], v[82:83], v[148:149], v[82:83]
	v_pk_fma_f32 v[150:151], v[84:85], v[150:151], v[84:85]
	v_pk_mul_f32 v[144:145], v[144:145], v[190:191]
	v_pk_mul_f32 v[146:147], v[146:147], v[190:191]
	v_pk_mul_f32 v[148:149], v[148:149], v[190:191]
	v_pk_mul_f32 v[150:151], v[150:151], v[190:191]
	v_pk_mul_f32 v[144:145], v[144:145], v[186:187]
	v_pk_mul_f32 v[146:147], v[146:147], v[186:187]
	v_pk_mul_f32 v[148:149], v[148:149], v[186:187]
	v_pk_mul_f32 v[150:151], v[150:151], v[186:187]
	v_exp_f32_e32 v144, v144
	v_exp_f32_e32 v145, v145
	v_exp_f32_e32 v146, v146
	v_exp_f32_e32 v147, v147
	v_exp_f32_e32 v148, v148
	v_exp_f32_e32 v149, v149
	v_exp_f32_e32 v150, v150
	v_exp_f32_e32 v151, v151
	s_nop 0
	v_pk_add_f32 v[144:145], v[144:145], v[184:185]
	v_pk_add_f32 v[146:147], v[146:147], v[184:185]
	v_pk_add_f32 v[148:149], v[148:149], v[184:185]
	v_pk_add_f32 v[150:151], v[150:151], v[184:185]
	v_rcp_f32_e32 v144, v144
	v_rcp_f32_e32 v145, v145
	v_rcp_f32_e32 v146, v146
	v_rcp_f32_e32 v147, v147
	v_rcp_f32_e32 v148, v148
	v_rcp_f32_e32 v149, v149
	v_rcp_f32_e32 v150, v150
	v_rcp_f32_e32 v151, v151
	s_nop 0
	v_pk_mul_f32 v[86:87], v[86:87], v[144:145]
	v_pk_mul_f32 v[88:89], v[88:89], v[146:147]
	v_pk_mul_f32 v[82:83], v[82:83], v[148:149]
	v_pk_mul_f32 v[84:85], v[84:85], v[150:151]
	v_cvt_pk_bf16_f32 v86, v86, v87
	v_cvt_pk_bf16_f32 v87, v88, v89
	v_cvt_pk_bf16_f32 v88, v82, v83
	v_cvt_pk_bf16_f32 v89, v84, v85
	v_mov_b32_e32 v158, v86
	v_mov_b32_e32 v159, v87
	v_mov_b32_e32 v160, v88
	v_mov_b32_e32 v161, v89
	v_mov_b32_dpp v86, v94 row_shl:8 row_mask:0xf bank_mask:0x3
	v_mov_b32_dpp v87, v95 row_shl:8 row_mask:0xf bank_mask:0x3
	v_mov_b32_dpp v88, v96 row_shl:8 row_mask:0xf bank_mask:0x3
	v_mov_b32_dpp v89, v97 row_shl:8 row_mask:0xf bank_mask:0x3
	v_mov_b32_dpp v94, v158 row_shr:8 row_mask:0xf bank_mask:0xc
	v_mov_b32_dpp v95, v159 row_shr:8 row_mask:0xf bank_mask:0xc
	v_mov_b32_dpp v96, v160 row_shr:8 row_mask:0xf bank_mask:0xc
	v_mov_b32_dpp v97, v161 row_shr:8 row_mask:0xf bank_mask:0xc
	s_mul_i32 s28, s22, 32
	v_lshl_add_u64 v[180:181], s[28:29], 0, v[178:179]
	global_store_dwordx4 v[180:181], v[94:97], off
	s_mul_i32 s28, s22, 40
	v_lshl_add_u64 v[180:181], s[28:29], 0, v[178:179]
	global_store_dwordx4 v[180:181], v[86:89], off
	v_pk_mul_f32 v[78:79], v[78:79], v[242:243] op_sel:[0,1] op_sel_hi:[1,1]
	v_pk_mul_f32 v[80:81], v[80:81], v[242:243] op_sel:[0,1] op_sel_hi:[1,1]
	v_pk_mul_f32 v[74:75], v[74:75], v[242:243] op_sel:[0,1] op_sel_hi:[1,1]
	v_pk_mul_f32 v[76:77], v[76:77], v[242:243] op_sel:[0,1] op_sel_hi:[1,1]
	v_pk_mul_f32 v[144:145], v[78:79], v[188:189]
	v_pk_mul_f32 v[146:147], v[80:81], v[188:189]
	v_pk_mul_f32 v[148:149], v[74:75], v[188:189]
	v_pk_mul_f32 v[150:151], v[76:77], v[188:189]
	v_pk_mul_f32 v[144:145], v[78:79], v[144:145]
	v_pk_mul_f32 v[146:147], v[80:81], v[146:147]
	v_pk_mul_f32 v[148:149], v[74:75], v[148:149]
	v_pk_mul_f32 v[150:151], v[76:77], v[150:151]
	v_pk_fma_f32 v[144:145], v[78:79], v[144:145], v[78:79]
	v_pk_fma_f32 v[146:147], v[80:81], v[146:147], v[80:81]
	v_pk_fma_f32 v[148:149], v[74:75], v[148:149], v[74:75]
	v_pk_fma_f32 v[150:151], v[76:77], v[150:151], v[76:77]
	v_pk_mul_f32 v[144:145], v[144:145], v[190:191]
	v_pk_mul_f32 v[146:147], v[146:147], v[190:191]
	v_pk_mul_f32 v[148:149], v[148:149], v[190:191]
	v_pk_mul_f32 v[150:151], v[150:151], v[190:191]
	v_pk_mul_f32 v[144:145], v[144:145], v[186:187]
	v_pk_mul_f32 v[146:147], v[146:147], v[186:187]
	v_pk_mul_f32 v[148:149], v[148:149], v[186:187]
	v_pk_mul_f32 v[150:151], v[150:151], v[186:187]
	v_exp_f32_e32 v144, v144
	v_exp_f32_e32 v145, v145
	v_exp_f32_e32 v146, v146
	v_exp_f32_e32 v147, v147
	v_exp_f32_e32 v148, v148
	v_exp_f32_e32 v149, v149
	v_exp_f32_e32 v150, v150
	v_exp_f32_e32 v151, v151
	s_nop 0
	v_pk_add_f32 v[144:145], v[144:145], v[184:185]
	v_pk_add_f32 v[146:147], v[146:147], v[184:185]
	v_pk_add_f32 v[148:149], v[148:149], v[184:185]
	v_pk_add_f32 v[150:151], v[150:151], v[184:185]
	v_rcp_f32_e32 v144, v144
	v_rcp_f32_e32 v145, v145
	v_rcp_f32_e32 v146, v146
	v_rcp_f32_e32 v147, v147
	v_rcp_f32_e32 v148, v148
	v_rcp_f32_e32 v149, v149
	v_rcp_f32_e32 v150, v150
	v_rcp_f32_e32 v151, v151
	s_nop 0
	v_pk_mul_f32 v[78:79], v[78:79], v[144:145]
	v_pk_mul_f32 v[80:81], v[80:81], v[146:147]
	v_pk_mul_f32 v[74:75], v[74:75], v[148:149]
	v_pk_mul_f32 v[76:77], v[76:77], v[150:151]
	v_cvt_pk_bf16_f32 v78, v78, v79
	v_cvt_pk_bf16_f32 v79, v80, v81
	v_cvt_pk_bf16_f32 v80, v74, v75
	v_cvt_pk_bf16_f32 v81, v76, v77
	v_pk_mul_f32 v[70:71], v[70:71], v[242:243] op_sel:[0,1] op_sel_hi:[1,1]
	v_pk_mul_f32 v[72:73], v[72:73], v[242:243] op_sel:[0,1] op_sel_hi:[1,1]
	v_pk_mul_f32 v[66:67], v[66:67], v[242:243] op_sel:[0,1] op_sel_hi:[1,1]
	v_pk_mul_f32 v[68:69], v[68:69], v[242:243] op_sel:[0,1] op_sel_hi:[1,1]
	v_pk_mul_f32 v[144:145], v[70:71], v[188:189]
	v_pk_mul_f32 v[146:147], v[72:73], v[188:189]
	v_pk_mul_f32 v[148:149], v[66:67], v[188:189]
	v_pk_mul_f32 v[150:151], v[68:69], v[188:189]
	v_pk_mul_f32 v[144:145], v[70:71], v[144:145]
	v_pk_mul_f32 v[146:147], v[72:73], v[146:147]
	v_pk_mul_f32 v[148:149], v[66:67], v[148:149]
	v_pk_mul_f32 v[150:151], v[68:69], v[150:151]
	v_pk_fma_f32 v[144:145], v[70:71], v[144:145], v[70:71]
	v_pk_fma_f32 v[146:147], v[72:73], v[146:147], v[72:73]
	v_pk_fma_f32 v[148:149], v[66:67], v[148:149], v[66:67]
	v_pk_fma_f32 v[150:151], v[68:69], v[150:151], v[68:69]
	v_pk_mul_f32 v[144:145], v[144:145], v[190:191]
	v_pk_mul_f32 v[146:147], v[146:147], v[190:191]
	v_pk_mul_f32 v[148:149], v[148:149], v[190:191]
	v_pk_mul_f32 v[150:151], v[150:151], v[190:191]
	v_pk_mul_f32 v[144:145], v[144:145], v[186:187]
	v_pk_mul_f32 v[146:147], v[146:147], v[186:187]
	v_pk_mul_f32 v[148:149], v[148:149], v[186:187]
	v_pk_mul_f32 v[150:151], v[150:151], v[186:187]
	v_exp_f32_e32 v144, v144
	v_exp_f32_e32 v145, v145
	v_exp_f32_e32 v146, v146
	v_exp_f32_e32 v147, v147
	v_exp_f32_e32 v148, v148
	v_exp_f32_e32 v149, v149
	v_exp_f32_e32 v150, v150
	v_exp_f32_e32 v151, v151
	s_nop 0
	v_pk_add_f32 v[144:145], v[144:145], v[184:185]
	v_pk_add_f32 v[146:147], v[146:147], v[184:185]
	v_pk_add_f32 v[148:149], v[148:149], v[184:185]
	v_pk_add_f32 v[150:151], v[150:151], v[184:185]
	v_rcp_f32_e32 v144, v144
	v_rcp_f32_e32 v145, v145
	v_rcp_f32_e32 v146, v146
	v_rcp_f32_e32 v147, v147
	v_rcp_f32_e32 v148, v148
	v_rcp_f32_e32 v149, v149
	v_rcp_f32_e32 v150, v150
	v_rcp_f32_e32 v151, v151
	s_nop 0
	v_pk_mul_f32 v[70:71], v[70:71], v[144:145]
	v_pk_mul_f32 v[72:73], v[72:73], v[146:147]
	v_pk_mul_f32 v[66:67], v[66:67], v[148:149]
	v_pk_mul_f32 v[68:69], v[68:69], v[150:151]
	v_cvt_pk_bf16_f32 v70, v70, v71
	v_cvt_pk_bf16_f32 v71, v72, v73
	v_cvt_pk_bf16_f32 v72, v66, v67
	v_cvt_pk_bf16_f32 v73, v68, v69
	v_mov_b32_e32 v158, v70
	v_mov_b32_e32 v159, v71
	v_mov_b32_e32 v160, v72
	v_mov_b32_e32 v161, v73
	v_mov_b32_dpp v70, v78 row_shl:8 row_mask:0xf bank_mask:0x3
	v_mov_b32_dpp v71, v79 row_shl:8 row_mask:0xf bank_mask:0x3
	v_mov_b32_dpp v72, v80 row_shl:8 row_mask:0xf bank_mask:0x3
	v_mov_b32_dpp v73, v81 row_shl:8 row_mask:0xf bank_mask:0x3
	v_mov_b32_dpp v78, v158 row_shr:8 row_mask:0xf bank_mask:0xc
	v_mov_b32_dpp v79, v159 row_shr:8 row_mask:0xf bank_mask:0xc
	v_mov_b32_dpp v80, v160 row_shr:8 row_mask:0xf bank_mask:0xc
	v_mov_b32_dpp v81, v161 row_shr:8 row_mask:0xf bank_mask:0xc
	s_mul_i32 s28, s22, 48
	v_lshl_add_u64 v[180:181], s[28:29], 0, v[178:179]
	global_store_dwordx4 v[180:181], v[78:81], off
	s_mul_i32 s28, s22, 56
	v_lshl_add_u64 v[180:181], s[28:29], 0, v[178:179]
	global_store_dwordx4 v[180:181], v[70:73], off
	v_pk_mul_f32 v[62:63], v[62:63], v[244:245] op_sel_hi:[1,0]
	v_pk_mul_f32 v[64:65], v[64:65], v[244:245] op_sel_hi:[1,0]
	v_pk_mul_f32 v[58:59], v[58:59], v[244:245] op_sel_hi:[1,0]
	v_pk_mul_f32 v[60:61], v[60:61], v[244:245] op_sel_hi:[1,0]
	v_pk_mul_f32 v[144:145], v[62:63], v[188:189]
	v_pk_mul_f32 v[146:147], v[64:65], v[188:189]
	v_pk_mul_f32 v[148:149], v[58:59], v[188:189]
	v_pk_mul_f32 v[150:151], v[60:61], v[188:189]
	v_pk_mul_f32 v[144:145], v[62:63], v[144:145]
	v_pk_mul_f32 v[146:147], v[64:65], v[146:147]
	v_pk_mul_f32 v[148:149], v[58:59], v[148:149]
	v_pk_mul_f32 v[150:151], v[60:61], v[150:151]
	v_pk_fma_f32 v[144:145], v[62:63], v[144:145], v[62:63]
	v_pk_fma_f32 v[146:147], v[64:65], v[146:147], v[64:65]
	v_pk_fma_f32 v[148:149], v[58:59], v[148:149], v[58:59]
	v_pk_fma_f32 v[150:151], v[60:61], v[150:151], v[60:61]
	v_pk_mul_f32 v[144:145], v[144:145], v[190:191]
	v_pk_mul_f32 v[146:147], v[146:147], v[190:191]
	v_pk_mul_f32 v[148:149], v[148:149], v[190:191]
	v_pk_mul_f32 v[150:151], v[150:151], v[190:191]
	v_pk_mul_f32 v[144:145], v[144:145], v[186:187]
	v_pk_mul_f32 v[146:147], v[146:147], v[186:187]
	v_pk_mul_f32 v[148:149], v[148:149], v[186:187]
	v_pk_mul_f32 v[150:151], v[150:151], v[186:187]
	v_exp_f32_e32 v144, v144
	v_exp_f32_e32 v145, v145
	v_exp_f32_e32 v146, v146
	v_exp_f32_e32 v147, v147
	v_exp_f32_e32 v148, v148
	v_exp_f32_e32 v149, v149
	v_exp_f32_e32 v150, v150
	v_exp_f32_e32 v151, v151
	s_nop 0
	v_pk_add_f32 v[144:145], v[144:145], v[184:185]
	v_pk_add_f32 v[146:147], v[146:147], v[184:185]
	v_pk_add_f32 v[148:149], v[148:149], v[184:185]
	v_pk_add_f32 v[150:151], v[150:151], v[184:185]
	v_rcp_f32_e32 v144, v144
	v_rcp_f32_e32 v145, v145
	v_rcp_f32_e32 v146, v146
	v_rcp_f32_e32 v147, v147
	v_rcp_f32_e32 v148, v148
	v_rcp_f32_e32 v149, v149
	v_rcp_f32_e32 v150, v150
	v_rcp_f32_e32 v151, v151
	s_nop 0
	v_pk_mul_f32 v[62:63], v[62:63], v[144:145]
	v_pk_mul_f32 v[64:65], v[64:65], v[146:147]
	v_pk_mul_f32 v[58:59], v[58:59], v[148:149]
	v_pk_mul_f32 v[60:61], v[60:61], v[150:151]
	v_cvt_pk_bf16_f32 v62, v62, v63
	v_cvt_pk_bf16_f32 v63, v64, v65
	v_cvt_pk_bf16_f32 v64, v58, v59
	v_cvt_pk_bf16_f32 v65, v60, v61
	v_pk_mul_f32 v[54:55], v[54:55], v[244:245] op_sel_hi:[1,0]
	v_pk_mul_f32 v[56:57], v[56:57], v[244:245] op_sel_hi:[1,0]
	v_pk_mul_f32 v[50:51], v[50:51], v[244:245] op_sel_hi:[1,0]
	v_pk_mul_f32 v[52:53], v[52:53], v[244:245] op_sel_hi:[1,0]
	v_pk_mul_f32 v[144:145], v[54:55], v[188:189]
	v_pk_mul_f32 v[146:147], v[56:57], v[188:189]
	v_pk_mul_f32 v[148:149], v[50:51], v[188:189]
	v_pk_mul_f32 v[150:151], v[52:53], v[188:189]
	v_pk_mul_f32 v[144:145], v[54:55], v[144:145]
	v_pk_mul_f32 v[146:147], v[56:57], v[146:147]
	v_pk_mul_f32 v[148:149], v[50:51], v[148:149]
	v_pk_mul_f32 v[150:151], v[52:53], v[150:151]
	v_pk_fma_f32 v[144:145], v[54:55], v[144:145], v[54:55]
	v_pk_fma_f32 v[146:147], v[56:57], v[146:147], v[56:57]
	v_pk_fma_f32 v[148:149], v[50:51], v[148:149], v[50:51]
	v_pk_fma_f32 v[150:151], v[52:53], v[150:151], v[52:53]
	v_pk_mul_f32 v[144:145], v[144:145], v[190:191]
	v_pk_mul_f32 v[146:147], v[146:147], v[190:191]
	v_pk_mul_f32 v[148:149], v[148:149], v[190:191]
	v_pk_mul_f32 v[150:151], v[150:151], v[190:191]
	v_pk_mul_f32 v[144:145], v[144:145], v[186:187]
	v_pk_mul_f32 v[146:147], v[146:147], v[186:187]
	v_pk_mul_f32 v[148:149], v[148:149], v[186:187]
	v_pk_mul_f32 v[150:151], v[150:151], v[186:187]
	v_exp_f32_e32 v144, v144
	v_exp_f32_e32 v145, v145
	v_exp_f32_e32 v146, v146
	v_exp_f32_e32 v147, v147
	v_exp_f32_e32 v148, v148
	v_exp_f32_e32 v149, v149
	v_exp_f32_e32 v150, v150
	v_exp_f32_e32 v151, v151
	s_nop 0
	v_pk_add_f32 v[144:145], v[144:145], v[184:185]
	v_pk_add_f32 v[146:147], v[146:147], v[184:185]
	v_pk_add_f32 v[148:149], v[148:149], v[184:185]
	v_pk_add_f32 v[150:151], v[150:151], v[184:185]
	v_rcp_f32_e32 v144, v144
	v_rcp_f32_e32 v145, v145
	v_rcp_f32_e32 v146, v146
	v_rcp_f32_e32 v147, v147
	v_rcp_f32_e32 v148, v148
	v_rcp_f32_e32 v149, v149
	v_rcp_f32_e32 v150, v150
	v_rcp_f32_e32 v151, v151
	s_nop 0
	v_pk_mul_f32 v[54:55], v[54:55], v[144:145]
	v_pk_mul_f32 v[56:57], v[56:57], v[146:147]
	v_pk_mul_f32 v[50:51], v[50:51], v[148:149]
	v_pk_mul_f32 v[52:53], v[52:53], v[150:151]
	v_cvt_pk_bf16_f32 v54, v54, v55
	v_cvt_pk_bf16_f32 v55, v56, v57
	v_cvt_pk_bf16_f32 v56, v50, v51
	v_cvt_pk_bf16_f32 v57, v52, v53
	v_mov_b32_e32 v158, v54
	v_mov_b32_e32 v159, v55
	v_mov_b32_e32 v160, v56
	v_mov_b32_e32 v161, v57
	v_mov_b32_dpp v54, v62 row_shl:8 row_mask:0xf bank_mask:0x3
	v_mov_b32_dpp v55, v63 row_shl:8 row_mask:0xf bank_mask:0x3
	v_mov_b32_dpp v56, v64 row_shl:8 row_mask:0xf bank_mask:0x3
	v_mov_b32_dpp v57, v65 row_shl:8 row_mask:0xf bank_mask:0x3
	v_mov_b32_dpp v62, v158 row_shr:8 row_mask:0xf bank_mask:0xc
	v_mov_b32_dpp v63, v159 row_shr:8 row_mask:0xf bank_mask:0xc
	v_mov_b32_dpp v64, v160 row_shr:8 row_mask:0xf bank_mask:0xc
	v_mov_b32_dpp v65, v161 row_shr:8 row_mask:0xf bank_mask:0xc
	s_mul_i32 s28, s22, 128
	v_lshl_add_u64 v[180:181], s[28:29], 0, v[178:179]
	global_store_dwordx4 v[180:181], v[62:65], off
	s_mul_i32 s28, s22, 136
	v_lshl_add_u64 v[180:181], s[28:29], 0, v[178:179]
	global_store_dwordx4 v[180:181], v[54:57], off
	v_pk_mul_f32 v[46:47], v[46:47], v[244:245] op_sel:[0,1] op_sel_hi:[1,1]
	v_pk_mul_f32 v[48:49], v[48:49], v[244:245] op_sel:[0,1] op_sel_hi:[1,1]
	v_pk_mul_f32 v[42:43], v[42:43], v[244:245] op_sel:[0,1] op_sel_hi:[1,1]
	v_pk_mul_f32 v[44:45], v[44:45], v[244:245] op_sel:[0,1] op_sel_hi:[1,1]
	v_pk_mul_f32 v[144:145], v[46:47], v[188:189]
	v_pk_mul_f32 v[146:147], v[48:49], v[188:189]
	v_pk_mul_f32 v[148:149], v[42:43], v[188:189]
	v_pk_mul_f32 v[150:151], v[44:45], v[188:189]
	v_pk_mul_f32 v[144:145], v[46:47], v[144:145]
	v_pk_mul_f32 v[146:147], v[48:49], v[146:147]
	v_pk_mul_f32 v[148:149], v[42:43], v[148:149]
	v_pk_mul_f32 v[150:151], v[44:45], v[150:151]
	v_pk_fma_f32 v[144:145], v[46:47], v[144:145], v[46:47]
	v_pk_fma_f32 v[146:147], v[48:49], v[146:147], v[48:49]
	v_pk_fma_f32 v[148:149], v[42:43], v[148:149], v[42:43]
	v_pk_fma_f32 v[150:151], v[44:45], v[150:151], v[44:45]
	v_pk_mul_f32 v[144:145], v[144:145], v[190:191]
	v_pk_mul_f32 v[146:147], v[146:147], v[190:191]
	v_pk_mul_f32 v[148:149], v[148:149], v[190:191]
	v_pk_mul_f32 v[150:151], v[150:151], v[190:191]
	v_pk_mul_f32 v[144:145], v[144:145], v[186:187]
	v_pk_mul_f32 v[146:147], v[146:147], v[186:187]
	v_pk_mul_f32 v[148:149], v[148:149], v[186:187]
	v_pk_mul_f32 v[150:151], v[150:151], v[186:187]
	v_exp_f32_e32 v144, v144
	v_exp_f32_e32 v145, v145
	v_exp_f32_e32 v146, v146
	v_exp_f32_e32 v147, v147
	v_exp_f32_e32 v148, v148
	v_exp_f32_e32 v149, v149
	v_exp_f32_e32 v150, v150
	v_exp_f32_e32 v151, v151
	s_nop 0
	v_pk_add_f32 v[144:145], v[144:145], v[184:185]
	v_pk_add_f32 v[146:147], v[146:147], v[184:185]
	v_pk_add_f32 v[148:149], v[148:149], v[184:185]
	v_pk_add_f32 v[150:151], v[150:151], v[184:185]
	v_rcp_f32_e32 v144, v144
	v_rcp_f32_e32 v145, v145
	v_rcp_f32_e32 v146, v146
	v_rcp_f32_e32 v147, v147
	v_rcp_f32_e32 v148, v148
	v_rcp_f32_e32 v149, v149
	v_rcp_f32_e32 v150, v150
	v_rcp_f32_e32 v151, v151
	s_nop 0
	v_pk_mul_f32 v[46:47], v[46:47], v[144:145]
	v_pk_mul_f32 v[48:49], v[48:49], v[146:147]
	v_pk_mul_f32 v[42:43], v[42:43], v[148:149]
	v_pk_mul_f32 v[44:45], v[44:45], v[150:151]
	v_cvt_pk_bf16_f32 v46, v46, v47
	v_cvt_pk_bf16_f32 v47, v48, v49
	v_cvt_pk_bf16_f32 v48, v42, v43
	v_cvt_pk_bf16_f32 v49, v44, v45
	v_pk_mul_f32 v[38:39], v[38:39], v[244:245] op_sel:[0,1] op_sel_hi:[1,1]
	v_pk_mul_f32 v[40:41], v[40:41], v[244:245] op_sel:[0,1] op_sel_hi:[1,1]
	v_pk_mul_f32 v[34:35], v[34:35], v[244:245] op_sel:[0,1] op_sel_hi:[1,1]
	v_pk_mul_f32 v[36:37], v[36:37], v[244:245] op_sel:[0,1] op_sel_hi:[1,1]
	v_pk_mul_f32 v[144:145], v[38:39], v[188:189]
	v_pk_mul_f32 v[146:147], v[40:41], v[188:189]
	v_pk_mul_f32 v[148:149], v[34:35], v[188:189]
	v_pk_mul_f32 v[150:151], v[36:37], v[188:189]
	v_pk_mul_f32 v[144:145], v[38:39], v[144:145]
	v_pk_mul_f32 v[146:147], v[40:41], v[146:147]
	v_pk_mul_f32 v[148:149], v[34:35], v[148:149]
	v_pk_mul_f32 v[150:151], v[36:37], v[150:151]
	v_pk_fma_f32 v[144:145], v[38:39], v[144:145], v[38:39]
	v_pk_fma_f32 v[146:147], v[40:41], v[146:147], v[40:41]
	v_pk_fma_f32 v[148:149], v[34:35], v[148:149], v[34:35]
	v_pk_fma_f32 v[150:151], v[36:37], v[150:151], v[36:37]
	v_pk_mul_f32 v[144:145], v[144:145], v[190:191]
	v_pk_mul_f32 v[146:147], v[146:147], v[190:191]
	v_pk_mul_f32 v[148:149], v[148:149], v[190:191]
	v_pk_mul_f32 v[150:151], v[150:151], v[190:191]
	v_pk_mul_f32 v[144:145], v[144:145], v[186:187]
	v_pk_mul_f32 v[146:147], v[146:147], v[186:187]
	v_pk_mul_f32 v[148:149], v[148:149], v[186:187]
	v_pk_mul_f32 v[150:151], v[150:151], v[186:187]
	v_exp_f32_e32 v144, v144
	v_exp_f32_e32 v145, v145
	v_exp_f32_e32 v146, v146
	v_exp_f32_e32 v147, v147
	v_exp_f32_e32 v148, v148
	v_exp_f32_e32 v149, v149
	v_exp_f32_e32 v150, v150
	v_exp_f32_e32 v151, v151
	s_nop 0
	v_pk_add_f32 v[144:145], v[144:145], v[184:185]
	v_pk_add_f32 v[146:147], v[146:147], v[184:185]
	v_pk_add_f32 v[148:149], v[148:149], v[184:185]
	v_pk_add_f32 v[150:151], v[150:151], v[184:185]
	v_rcp_f32_e32 v144, v144
	v_rcp_f32_e32 v145, v145
	v_rcp_f32_e32 v146, v146
	v_rcp_f32_e32 v147, v147
	v_rcp_f32_e32 v148, v148
	v_rcp_f32_e32 v149, v149
	v_rcp_f32_e32 v150, v150
	v_rcp_f32_e32 v151, v151
	s_nop 0
	v_pk_mul_f32 v[38:39], v[38:39], v[144:145]
	v_pk_mul_f32 v[40:41], v[40:41], v[146:147]
	v_pk_mul_f32 v[34:35], v[34:35], v[148:149]
	v_pk_mul_f32 v[36:37], v[36:37], v[150:151]
	v_cvt_pk_bf16_f32 v38, v38, v39
	v_cvt_pk_bf16_f32 v39, v40, v41
	v_cvt_pk_bf16_f32 v40, v34, v35
	v_cvt_pk_bf16_f32 v41, v36, v37
	v_mov_b32_e32 v158, v38
	v_mov_b32_e32 v159, v39
	v_mov_b32_e32 v160, v40
	v_mov_b32_e32 v161, v41
	v_mov_b32_dpp v38, v46 row_shl:8 row_mask:0xf bank_mask:0x3
	v_mov_b32_dpp v39, v47 row_shl:8 row_mask:0xf bank_mask:0x3
	v_mov_b32_dpp v40, v48 row_shl:8 row_mask:0xf bank_mask:0x3
	v_mov_b32_dpp v41, v49 row_shl:8 row_mask:0xf bank_mask:0x3
	v_mov_b32_dpp v46, v158 row_shr:8 row_mask:0xf bank_mask:0xc
	v_mov_b32_dpp v47, v159 row_shr:8 row_mask:0xf bank_mask:0xc
	v_mov_b32_dpp v48, v160 row_shr:8 row_mask:0xf bank_mask:0xc
	v_mov_b32_dpp v49, v161 row_shr:8 row_mask:0xf bank_mask:0xc
	s_mul_i32 s28, s22, 144
	v_lshl_add_u64 v[180:181], s[28:29], 0, v[178:179]
	global_store_dwordx4 v[180:181], v[46:49], off
	s_mul_i32 s28, s22, 152
	v_lshl_add_u64 v[180:181], s[28:29], 0, v[178:179]
	global_store_dwordx4 v[180:181], v[38:41], off
	v_pk_mul_f32 v[30:31], v[30:31], v[246:247] op_sel_hi:[1,0]
	v_pk_mul_f32 v[32:33], v[32:33], v[246:247] op_sel_hi:[1,0]
	v_pk_mul_f32 v[26:27], v[26:27], v[246:247] op_sel_hi:[1,0]
	v_pk_mul_f32 v[28:29], v[28:29], v[246:247] op_sel_hi:[1,0]
	v_pk_mul_f32 v[144:145], v[30:31], v[188:189]
	v_pk_mul_f32 v[146:147], v[32:33], v[188:189]
	v_pk_mul_f32 v[148:149], v[26:27], v[188:189]
	v_pk_mul_f32 v[150:151], v[28:29], v[188:189]
	v_pk_mul_f32 v[144:145], v[30:31], v[144:145]
	v_pk_mul_f32 v[146:147], v[32:33], v[146:147]
	v_pk_mul_f32 v[148:149], v[26:27], v[148:149]
	v_pk_mul_f32 v[150:151], v[28:29], v[150:151]
	v_pk_fma_f32 v[144:145], v[30:31], v[144:145], v[30:31]
	v_pk_fma_f32 v[146:147], v[32:33], v[146:147], v[32:33]
	v_pk_fma_f32 v[148:149], v[26:27], v[148:149], v[26:27]
	v_pk_fma_f32 v[150:151], v[28:29], v[150:151], v[28:29]
	v_pk_mul_f32 v[144:145], v[144:145], v[190:191]
	v_pk_mul_f32 v[146:147], v[146:147], v[190:191]
	v_pk_mul_f32 v[148:149], v[148:149], v[190:191]
	v_pk_mul_f32 v[150:151], v[150:151], v[190:191]
	v_pk_mul_f32 v[144:145], v[144:145], v[186:187]
	v_pk_mul_f32 v[146:147], v[146:147], v[186:187]
	v_pk_mul_f32 v[148:149], v[148:149], v[186:187]
	v_pk_mul_f32 v[150:151], v[150:151], v[186:187]
	v_exp_f32_e32 v144, v144
	v_exp_f32_e32 v145, v145
	v_exp_f32_e32 v146, v146
	v_exp_f32_e32 v147, v147
	v_exp_f32_e32 v148, v148
	v_exp_f32_e32 v149, v149
	v_exp_f32_e32 v150, v150
	v_exp_f32_e32 v151, v151
	s_nop 0
	v_pk_add_f32 v[144:145], v[144:145], v[184:185]
	v_pk_add_f32 v[146:147], v[146:147], v[184:185]
	v_pk_add_f32 v[148:149], v[148:149], v[184:185]
	v_pk_add_f32 v[150:151], v[150:151], v[184:185]
	v_rcp_f32_e32 v144, v144
	v_rcp_f32_e32 v145, v145
	v_rcp_f32_e32 v146, v146
	v_rcp_f32_e32 v147, v147
	v_rcp_f32_e32 v148, v148
	v_rcp_f32_e32 v149, v149
	v_rcp_f32_e32 v150, v150
	v_rcp_f32_e32 v151, v151
	s_nop 0
	v_pk_mul_f32 v[30:31], v[30:31], v[144:145]
	v_pk_mul_f32 v[32:33], v[32:33], v[146:147]
	v_pk_mul_f32 v[26:27], v[26:27], v[148:149]
	v_pk_mul_f32 v[28:29], v[28:29], v[150:151]
	v_cvt_pk_bf16_f32 v30, v30, v31
	v_cvt_pk_bf16_f32 v31, v32, v33
	v_cvt_pk_bf16_f32 v32, v26, v27
	v_cvt_pk_bf16_f32 v33, v28, v29
	v_pk_mul_f32 v[22:23], v[22:23], v[246:247] op_sel_hi:[1,0]
	v_pk_mul_f32 v[24:25], v[24:25], v[246:247] op_sel_hi:[1,0]
	v_pk_mul_f32 v[18:19], v[18:19], v[246:247] op_sel_hi:[1,0]
	v_pk_mul_f32 v[20:21], v[20:21], v[246:247] op_sel_hi:[1,0]
	v_pk_mul_f32 v[144:145], v[22:23], v[188:189]
	v_pk_mul_f32 v[146:147], v[24:25], v[188:189]
	v_pk_mul_f32 v[148:149], v[18:19], v[188:189]
	v_pk_mul_f32 v[150:151], v[20:21], v[188:189]
	v_pk_mul_f32 v[144:145], v[22:23], v[144:145]
	v_pk_mul_f32 v[146:147], v[24:25], v[146:147]
	v_pk_mul_f32 v[148:149], v[18:19], v[148:149]
	v_pk_mul_f32 v[150:151], v[20:21], v[150:151]
	v_pk_fma_f32 v[144:145], v[22:23], v[144:145], v[22:23]
	v_pk_fma_f32 v[146:147], v[24:25], v[146:147], v[24:25]
	v_pk_fma_f32 v[148:149], v[18:19], v[148:149], v[18:19]
	v_pk_fma_f32 v[150:151], v[20:21], v[150:151], v[20:21]
	v_pk_mul_f32 v[144:145], v[144:145], v[190:191]
	v_pk_mul_f32 v[146:147], v[146:147], v[190:191]
	v_pk_mul_f32 v[148:149], v[148:149], v[190:191]
	v_pk_mul_f32 v[150:151], v[150:151], v[190:191]
	v_pk_mul_f32 v[144:145], v[144:145], v[186:187]
	v_pk_mul_f32 v[146:147], v[146:147], v[186:187]
	v_pk_mul_f32 v[148:149], v[148:149], v[186:187]
	v_pk_mul_f32 v[150:151], v[150:151], v[186:187]
	v_exp_f32_e32 v144, v144
	v_exp_f32_e32 v145, v145
	v_exp_f32_e32 v146, v146
	v_exp_f32_e32 v147, v147
	v_exp_f32_e32 v148, v148
	v_exp_f32_e32 v149, v149
	v_exp_f32_e32 v150, v150
	v_exp_f32_e32 v151, v151
	s_nop 0
	v_pk_add_f32 v[144:145], v[144:145], v[184:185]
	v_pk_add_f32 v[146:147], v[146:147], v[184:185]
	v_pk_add_f32 v[148:149], v[148:149], v[184:185]
	v_pk_add_f32 v[150:151], v[150:151], v[184:185]
	v_rcp_f32_e32 v144, v144
	v_rcp_f32_e32 v145, v145
	v_rcp_f32_e32 v146, v146
	v_rcp_f32_e32 v147, v147
	v_rcp_f32_e32 v148, v148
	v_rcp_f32_e32 v149, v149
	v_rcp_f32_e32 v150, v150
	v_rcp_f32_e32 v151, v151
	s_nop 0
	v_pk_mul_f32 v[22:23], v[22:23], v[144:145]
	v_pk_mul_f32 v[24:25], v[24:25], v[146:147]
	v_pk_mul_f32 v[18:19], v[18:19], v[148:149]
	v_pk_mul_f32 v[20:21], v[20:21], v[150:151]
	v_cvt_pk_bf16_f32 v22, v22, v23
	v_cvt_pk_bf16_f32 v23, v24, v25
	v_cvt_pk_bf16_f32 v24, v18, v19
	v_cvt_pk_bf16_f32 v25, v20, v21
	v_mov_b32_e32 v158, v22
	v_mov_b32_e32 v159, v23
	v_mov_b32_e32 v160, v24
	v_mov_b32_e32 v161, v25
	v_mov_b32_dpp v22, v30 row_shl:8 row_mask:0xf bank_mask:0x3
	v_mov_b32_dpp v23, v31 row_shl:8 row_mask:0xf bank_mask:0x3
	v_mov_b32_dpp v24, v32 row_shl:8 row_mask:0xf bank_mask:0x3
	v_mov_b32_dpp v25, v33 row_shl:8 row_mask:0xf bank_mask:0x3
	v_mov_b32_dpp v30, v158 row_shr:8 row_mask:0xf bank_mask:0xc
	v_mov_b32_dpp v31, v159 row_shr:8 row_mask:0xf bank_mask:0xc
	v_mov_b32_dpp v32, v160 row_shr:8 row_mask:0xf bank_mask:0xc
	v_mov_b32_dpp v33, v161 row_shr:8 row_mask:0xf bank_mask:0xc
	s_mul_i32 s28, s22, 160
	v_lshl_add_u64 v[180:181], s[28:29], 0, v[178:179]
	global_store_dwordx4 v[180:181], v[30:33], off
	s_mul_i32 s28, s22, 168
	v_lshl_add_u64 v[180:181], s[28:29], 0, v[178:179]
	global_store_dwordx4 v[180:181], v[22:25], off
	v_pk_mul_f32 v[14:15], v[14:15], v[246:247] op_sel:[0,1] op_sel_hi:[1,1]
	v_pk_mul_f32 v[16:17], v[16:17], v[246:247] op_sel:[0,1] op_sel_hi:[1,1]
	v_pk_mul_f32 v[10:11], v[10:11], v[246:247] op_sel:[0,1] op_sel_hi:[1,1]
	v_pk_mul_f32 v[12:13], v[12:13], v[246:247] op_sel:[0,1] op_sel_hi:[1,1]
	v_pk_mul_f32 v[144:145], v[14:15], v[188:189]
	v_pk_mul_f32 v[146:147], v[16:17], v[188:189]
	v_pk_mul_f32 v[148:149], v[10:11], v[188:189]
	v_pk_mul_f32 v[150:151], v[12:13], v[188:189]
	v_pk_mul_f32 v[144:145], v[14:15], v[144:145]
	v_pk_mul_f32 v[146:147], v[16:17], v[146:147]
	v_pk_mul_f32 v[148:149], v[10:11], v[148:149]
	v_pk_mul_f32 v[150:151], v[12:13], v[150:151]
	v_pk_fma_f32 v[144:145], v[14:15], v[144:145], v[14:15]
	v_pk_fma_f32 v[146:147], v[16:17], v[146:147], v[16:17]
	v_pk_fma_f32 v[148:149], v[10:11], v[148:149], v[10:11]
	v_pk_fma_f32 v[150:151], v[12:13], v[150:151], v[12:13]
	v_pk_mul_f32 v[144:145], v[144:145], v[190:191]
	v_pk_mul_f32 v[146:147], v[146:147], v[190:191]
	v_pk_mul_f32 v[148:149], v[148:149], v[190:191]
	v_pk_mul_f32 v[150:151], v[150:151], v[190:191]
	v_pk_mul_f32 v[144:145], v[144:145], v[186:187]
	v_pk_mul_f32 v[146:147], v[146:147], v[186:187]
	v_pk_mul_f32 v[148:149], v[148:149], v[186:187]
	v_pk_mul_f32 v[150:151], v[150:151], v[186:187]
	v_exp_f32_e32 v144, v144
	v_exp_f32_e32 v145, v145
	v_exp_f32_e32 v146, v146
	v_exp_f32_e32 v147, v147
	v_exp_f32_e32 v148, v148
	v_exp_f32_e32 v149, v149
	v_exp_f32_e32 v150, v150
	v_exp_f32_e32 v151, v151
	s_nop 0
	v_pk_add_f32 v[144:145], v[144:145], v[184:185]
	v_pk_add_f32 v[146:147], v[146:147], v[184:185]
	v_pk_add_f32 v[148:149], v[148:149], v[184:185]
	v_pk_add_f32 v[150:151], v[150:151], v[184:185]
	v_rcp_f32_e32 v144, v144
	v_rcp_f32_e32 v145, v145
	v_rcp_f32_e32 v146, v146
	v_rcp_f32_e32 v147, v147
	v_rcp_f32_e32 v148, v148
	v_rcp_f32_e32 v149, v149
	v_rcp_f32_e32 v150, v150
	v_rcp_f32_e32 v151, v151
	s_nop 0
	v_pk_mul_f32 v[14:15], v[14:15], v[144:145]
	v_pk_mul_f32 v[16:17], v[16:17], v[146:147]
	v_pk_mul_f32 v[10:11], v[10:11], v[148:149]
	v_pk_mul_f32 v[12:13], v[12:13], v[150:151]
	v_cvt_pk_bf16_f32 v14, v14, v15
	v_cvt_pk_bf16_f32 v15, v16, v17
	v_cvt_pk_bf16_f32 v16, v10, v11
	v_cvt_pk_bf16_f32 v17, v12, v13
	v_pk_mul_f32 v[6:7], v[6:7], v[246:247] op_sel:[0,1] op_sel_hi:[1,1]
	v_pk_mul_f32 v[8:9], v[8:9], v[246:247] op_sel:[0,1] op_sel_hi:[1,1]
	v_pk_mul_f32 v[2:3], v[2:3], v[246:247] op_sel:[0,1] op_sel_hi:[1,1]
	v_pk_mul_f32 v[4:5], v[4:5], v[246:247] op_sel:[0,1] op_sel_hi:[1,1]
	v_pk_mul_f32 v[144:145], v[6:7], v[188:189]
	v_pk_mul_f32 v[146:147], v[8:9], v[188:189]
	v_pk_mul_f32 v[148:149], v[2:3], v[188:189]
	v_pk_mul_f32 v[150:151], v[4:5], v[188:189]
	v_pk_mul_f32 v[144:145], v[6:7], v[144:145]
	v_pk_mul_f32 v[146:147], v[8:9], v[146:147]
	v_pk_mul_f32 v[148:149], v[2:3], v[148:149]
	v_pk_mul_f32 v[150:151], v[4:5], v[150:151]
	v_pk_fma_f32 v[144:145], v[6:7], v[144:145], v[6:7]
	v_pk_fma_f32 v[146:147], v[8:9], v[146:147], v[8:9]
	v_pk_fma_f32 v[148:149], v[2:3], v[148:149], v[2:3]
	v_pk_fma_f32 v[150:151], v[4:5], v[150:151], v[4:5]
	v_pk_mul_f32 v[144:145], v[144:145], v[190:191]
	v_pk_mul_f32 v[146:147], v[146:147], v[190:191]
	v_pk_mul_f32 v[148:149], v[148:149], v[190:191]
	v_pk_mul_f32 v[150:151], v[150:151], v[190:191]
	v_pk_mul_f32 v[144:145], v[144:145], v[186:187]
	v_pk_mul_f32 v[146:147], v[146:147], v[186:187]
	v_pk_mul_f32 v[148:149], v[148:149], v[186:187]
	v_pk_mul_f32 v[150:151], v[150:151], v[186:187]
	v_exp_f32_e32 v144, v144
	v_exp_f32_e32 v145, v145
	v_exp_f32_e32 v146, v146
	v_exp_f32_e32 v147, v147
	v_exp_f32_e32 v148, v148
	v_exp_f32_e32 v149, v149
	v_exp_f32_e32 v150, v150
	v_exp_f32_e32 v151, v151
	s_nop 0
	v_pk_add_f32 v[144:145], v[144:145], v[184:185]
	v_pk_add_f32 v[146:147], v[146:147], v[184:185]
	v_pk_add_f32 v[148:149], v[148:149], v[184:185]
	v_pk_add_f32 v[150:151], v[150:151], v[184:185]
	v_rcp_f32_e32 v144, v144
	v_rcp_f32_e32 v145, v145
	v_rcp_f32_e32 v146, v146
	v_rcp_f32_e32 v147, v147
	v_rcp_f32_e32 v148, v148
	v_rcp_f32_e32 v149, v149
	v_rcp_f32_e32 v150, v150
	v_rcp_f32_e32 v151, v151
	s_nop 0
	v_pk_mul_f32 v[6:7], v[6:7], v[144:145]
	v_pk_mul_f32 v[8:9], v[8:9], v[146:147]
	v_pk_mul_f32 v[2:3], v[2:3], v[148:149]
	v_pk_mul_f32 v[4:5], v[4:5], v[150:151]
	v_cvt_pk_bf16_f32 v6, v6, v7
	v_cvt_pk_bf16_f32 v7, v8, v9
	v_cvt_pk_bf16_f32 v8, v2, v3
	v_cvt_pk_bf16_f32 v9, v4, v5
	v_mov_b32_e32 v158, v6
	v_mov_b32_e32 v159, v7
	v_mov_b32_e32 v160, v8
	v_mov_b32_e32 v161, v9
	v_mov_b32_dpp v6, v14 row_shl:8 row_mask:0xf bank_mask:0x3
	v_mov_b32_dpp v7, v15 row_shl:8 row_mask:0xf bank_mask:0x3
	v_mov_b32_dpp v8, v16 row_shl:8 row_mask:0xf bank_mask:0x3
	v_mov_b32_dpp v9, v17 row_shl:8 row_mask:0xf bank_mask:0x3
	v_mov_b32_dpp v14, v158 row_shr:8 row_mask:0xf bank_mask:0xc
	v_mov_b32_dpp v15, v159 row_shr:8 row_mask:0xf bank_mask:0xc
	v_mov_b32_dpp v16, v160 row_shr:8 row_mask:0xf bank_mask:0xc
	v_mov_b32_dpp v17, v161 row_shr:8 row_mask:0xf bank_mask:0xc
	s_mul_i32 s28, s22, 176
	v_lshl_add_u64 v[180:181], s[28:29], 0, v[178:179]
	global_store_dwordx4 v[180:181], v[14:17], off
	s_mul_i32 s28, s22, 184
	v_lshl_add_u64 v[180:181], s[28:29], 0, v[178:179]
	global_store_dwordx4 v[180:181], v[6:9], off
	s_branch .Lpj_done
.Lpj_sigm:
	v_pk_mul_f32 v[126:127], v[126:127], v[240:241] op_sel_hi:[1,0]
	v_pk_mul_f32 v[128:129], v[128:129], v[240:241] op_sel_hi:[1,0]
	v_pk_mul_f32 v[122:123], v[122:123], v[240:241] op_sel_hi:[1,0]
	v_pk_mul_f32 v[124:125], v[124:125], v[240:241] op_sel_hi:[1,0]
	v_pk_mul_f32 v[144:145], v[126:127], v[186:187]
	v_pk_mul_f32 v[146:147], v[128:129], v[186:187]
	v_pk_mul_f32 v[148:149], v[122:123], v[186:187]
	v_pk_mul_f32 v[150:151], v[124:125], v[186:187]
	v_exp_f32_e32 v144, v144
	v_exp_f32_e32 v145, v145
	v_exp_f32_e32 v146, v146
	v_exp_f32_e32 v147, v147
	v_exp_f32_e32 v148, v148
	v_exp_f32_e32 v149, v149
	v_exp_f32_e32 v150, v150
	v_exp_f32_e32 v151, v151
	s_nop 0
	v_pk_add_f32 v[144:145], v[144:145], v[184:185]
	v_pk_add_f32 v[146:147], v[146:147], v[184:185]
	v_pk_add_f32 v[148:149], v[148:149], v[184:185]
	v_pk_add_f32 v[150:151], v[150:151], v[184:185]
	v_rcp_f32_e32 v144, v144
	v_rcp_f32_e32 v145, v145
	v_rcp_f32_e32 v146, v146
	v_rcp_f32_e32 v147, v147
	v_rcp_f32_e32 v148, v148
	v_rcp_f32_e32 v149, v149
	v_rcp_f32_e32 v150, v150
	v_rcp_f32_e32 v151, v151
	s_nop 0
	v_cvt_pk_bf16_f32 v126, v144, v145
	v_cvt_pk_bf16_f32 v127, v146, v147
	v_cvt_pk_bf16_f32 v128, v148, v149
	v_cvt_pk_bf16_f32 v129, v150, v151
	v_pk_mul_f32 v[118:119], v[118:119], v[240:241] op_sel_hi:[1,0]
	v_pk_mul_f32 v[120:121], v[120:121], v[240:241] op_sel_hi:[1,0]
	v_pk_mul_f32 v[114:115], v[114:115], v[240:241] op_sel_hi:[1,0]
	v_pk_mul_f32 v[116:117], v[116:117], v[240:241] op_sel_hi:[1,0]
	v_pk_mul_f32 v[144:145], v[118:119], v[186:187]
	v_pk_mul_f32 v[146:147], v[120:121], v[186:187]
	v_pk_mul_f32 v[148:149], v[114:115], v[186:187]
	v_pk_mul_f32 v[150:151], v[116:117], v[186:187]
	v_exp_f32_e32 v144, v144
	v_exp_f32_e32 v145, v145
	v_exp_f32_e32 v146, v146
	v_exp_f32_e32 v147, v147
	v_exp_f32_e32 v148, v148
	v_exp_f32_e32 v149, v149
	v_exp_f32_e32 v150, v150
	v_exp_f32_e32 v151, v151
	s_nop 0
	v_pk_add_f32 v[144:145], v[144:145], v[184:185]
	v_pk_add_f32 v[146:147], v[146:147], v[184:185]
	v_pk_add_f32 v[148:149], v[148:149], v[184:185]
	v_pk_add_f32 v[150:151], v[150:151], v[184:185]
	v_rcp_f32_e32 v144, v144
	v_rcp_f32_e32 v145, v145
	v_rcp_f32_e32 v146, v146
	v_rcp_f32_e32 v147, v147
	v_rcp_f32_e32 v148, v148
	v_rcp_f32_e32 v149, v149
	v_rcp_f32_e32 v150, v150
	v_rcp_f32_e32 v151, v151
	s_nop 0
	v_cvt_pk_bf16_f32 v118, v144, v145
	v_cvt_pk_bf16_f32 v119, v146, v147
	v_cvt_pk_bf16_f32 v120, v148, v149
	v_cvt_pk_bf16_f32 v121, v150, v151
	v_mov_b32_e32 v158, v118
	v_mov_b32_e32 v159, v119
	v_mov_b32_e32 v160, v120
	v_mov_b32_e32 v161, v121
	v_mov_b32_dpp v118, v126 row_shl:8 row_mask:0xf bank_mask:0x3
	v_mov_b32_dpp v119, v127 row_shl:8 row_mask:0xf bank_mask:0x3
	v_mov_b32_dpp v120, v128 row_shl:8 row_mask:0xf bank_mask:0x3
	v_mov_b32_dpp v121, v129 row_shl:8 row_mask:0xf bank_mask:0x3
	v_mov_b32_dpp v126, v158 row_shr:8 row_mask:0xf bank_mask:0xc
	v_mov_b32_dpp v127, v159 row_shr:8 row_mask:0xf bank_mask:0xc
	v_mov_b32_dpp v128, v160 row_shr:8 row_mask:0xf bank_mask:0xc
	v_mov_b32_dpp v129, v161 row_shr:8 row_mask:0xf bank_mask:0xc
	s_mul_i32 s28, s22, 0
	v_lshl_add_u64 v[180:181], s[28:29], 0, v[178:179]
	global_store_dwordx4 v[180:181], v[126:129], off
	s_mul_i32 s28, s22, 8
	v_lshl_add_u64 v[180:181], s[28:29], 0, v[178:179]
	global_store_dwordx4 v[180:181], v[118:121], off
	v_pk_mul_f32 v[110:111], v[110:111], v[240:241] op_sel:[0,1] op_sel_hi:[1,1]
	v_pk_mul_f32 v[112:113], v[112:113], v[240:241] op_sel:[0,1] op_sel_hi:[1,1]
	v_pk_mul_f32 v[106:107], v[106:107], v[240:241] op_sel:[0,1] op_sel_hi:[1,1]
	v_pk_mul_f32 v[108:109], v[108:109], v[240:241] op_sel:[0,1] op_sel_hi:[1,1]
	v_pk_mul_f32 v[144:145], v[110:111], v[186:187]
	v_pk_mul_f32 v[146:147], v[112:113], v[186:187]
	v_pk_mul_f32 v[148:149], v[106:107], v[186:187]
	v_pk_mul_f32 v[150:151], v[108:109], v[186:187]
	v_exp_f32_e32 v144, v144
	v_exp_f32_e32 v145, v145
	v_exp_f32_e32 v146, v146
	v_exp_f32_e32 v147, v147
	v_exp_f32_e32 v148, v148
	v_exp_f32_e32 v149, v149
	v_exp_f32_e32 v150, v150
	v_exp_f32_e32 v151, v151
	s_nop 0
	v_pk_add_f32 v[144:145], v[144:145], v[184:185]
	v_pk_add_f32 v[146:147], v[146:147], v[184:185]
	v_pk_add_f32 v[148:149], v[148:149], v[184:185]
	v_pk_add_f32 v[150:151], v[150:151], v[184:185]
	v_rcp_f32_e32 v144, v144
	v_rcp_f32_e32 v145, v145
	v_rcp_f32_e32 v146, v146
	v_rcp_f32_e32 v147, v147
	v_rcp_f32_e32 v148, v148
	v_rcp_f32_e32 v149, v149
	v_rcp_f32_e32 v150, v150
	v_rcp_f32_e32 v151, v151
	s_nop 0
	v_cvt_pk_bf16_f32 v110, v144, v145
	v_cvt_pk_bf16_f32 v111, v146, v147
	v_cvt_pk_bf16_f32 v112, v148, v149
	v_cvt_pk_bf16_f32 v113, v150, v151
	v_pk_mul_f32 v[102:103], v[102:103], v[240:241] op_sel:[0,1] op_sel_hi:[1,1]
	v_pk_mul_f32 v[104:105], v[104:105], v[240:241] op_sel:[0,1] op_sel_hi:[1,1]
	v_pk_mul_f32 v[98:99], v[98:99], v[240:241] op_sel:[0,1] op_sel_hi:[1,1]
	v_pk_mul_f32 v[100:101], v[100:101], v[240:241] op_sel:[0,1] op_sel_hi:[1,1]
	v_pk_mul_f32 v[144:145], v[102:103], v[186:187]
	v_pk_mul_f32 v[146:147], v[104:105], v[186:187]
	v_pk_mul_f32 v[148:149], v[98:99], v[186:187]
	v_pk_mul_f32 v[150:151], v[100:101], v[186:187]
	v_exp_f32_e32 v144, v144
	v_exp_f32_e32 v145, v145
	v_exp_f32_e32 v146, v146
	v_exp_f32_e32 v147, v147
	v_exp_f32_e32 v148, v148
	v_exp_f32_e32 v149, v149
	v_exp_f32_e32 v150, v150
	v_exp_f32_e32 v151, v151
	s_nop 0
	v_pk_add_f32 v[144:145], v[144:145], v[184:185]
	v_pk_add_f32 v[146:147], v[146:147], v[184:185]
	v_pk_add_f32 v[148:149], v[148:149], v[184:185]
	v_pk_add_f32 v[150:151], v[150:151], v[184:185]
	v_rcp_f32_e32 v144, v144
	v_rcp_f32_e32 v145, v145
	v_rcp_f32_e32 v146, v146
	v_rcp_f32_e32 v147, v147
	v_rcp_f32_e32 v148, v148
	v_rcp_f32_e32 v149, v149
	v_rcp_f32_e32 v150, v150
	v_rcp_f32_e32 v151, v151
	s_nop 0
	v_cvt_pk_bf16_f32 v102, v144, v145
	v_cvt_pk_bf16_f32 v103, v146, v147
	v_cvt_pk_bf16_f32 v104, v148, v149
	v_cvt_pk_bf16_f32 v105, v150, v151
	v_mov_b32_e32 v158, v102
	v_mov_b32_e32 v159, v103
	v_mov_b32_e32 v160, v104
	v_mov_b32_e32 v161, v105
	v_mov_b32_dpp v102, v110 row_shl:8 row_mask:0xf bank_mask:0x3
	v_mov_b32_dpp v103, v111 row_shl:8 row_mask:0xf bank_mask:0x3
	v_mov_b32_dpp v104, v112 row_shl:8 row_mask:0xf bank_mask:0x3
	v_mov_b32_dpp v105, v113 row_shl:8 row_mask:0xf bank_mask:0x3
	v_mov_b32_dpp v110, v158 row_shr:8 row_mask:0xf bank_mask:0xc
	v_mov_b32_dpp v111, v159 row_shr:8 row_mask:0xf bank_mask:0xc
	v_mov_b32_dpp v112, v160 row_shr:8 row_mask:0xf bank_mask:0xc
	v_mov_b32_dpp v113, v161 row_shr:8 row_mask:0xf bank_mask:0xc
	s_mul_i32 s28, s22, 16
	v_lshl_add_u64 v[180:181], s[28:29], 0, v[178:179]
	global_store_dwordx4 v[180:181], v[110:113], off
	s_mul_i32 s28, s22, 24
	v_lshl_add_u64 v[180:181], s[28:29], 0, v[178:179]
	global_store_dwordx4 v[180:181], v[102:105], off
	v_pk_mul_f32 v[94:95], v[94:95], v[242:243] op_sel_hi:[1,0]
	v_pk_mul_f32 v[96:97], v[96:97], v[242:243] op_sel_hi:[1,0]
	v_pk_mul_f32 v[90:91], v[90:91], v[242:243] op_sel_hi:[1,0]
	v_pk_mul_f32 v[92:93], v[92:93], v[242:243] op_sel_hi:[1,0]
	v_pk_mul_f32 v[144:145], v[94:95], v[186:187]
	v_pk_mul_f32 v[146:147], v[96:97], v[186:187]
	v_pk_mul_f32 v[148:149], v[90:91], v[186:187]
	v_pk_mul_f32 v[150:151], v[92:93], v[186:187]
	v_exp_f32_e32 v144, v144
	v_exp_f32_e32 v145, v145
	v_exp_f32_e32 v146, v146
	v_exp_f32_e32 v147, v147
	v_exp_f32_e32 v148, v148
	v_exp_f32_e32 v149, v149
	v_exp_f32_e32 v150, v150
	v_exp_f32_e32 v151, v151
	s_nop 0
	v_pk_add_f32 v[144:145], v[144:145], v[184:185]
	v_pk_add_f32 v[146:147], v[146:147], v[184:185]
	v_pk_add_f32 v[148:149], v[148:149], v[184:185]
	v_pk_add_f32 v[150:151], v[150:151], v[184:185]
	v_rcp_f32_e32 v144, v144
	v_rcp_f32_e32 v145, v145
	v_rcp_f32_e32 v146, v146
	v_rcp_f32_e32 v147, v147
	v_rcp_f32_e32 v148, v148
	v_rcp_f32_e32 v149, v149
	v_rcp_f32_e32 v150, v150
	v_rcp_f32_e32 v151, v151
	s_nop 0
	v_cvt_pk_bf16_f32 v94, v144, v145
	v_cvt_pk_bf16_f32 v95, v146, v147
	v_cvt_pk_bf16_f32 v96, v148, v149
	v_cvt_pk_bf16_f32 v97, v150, v151
	v_pk_mul_f32 v[86:87], v[86:87], v[242:243] op_sel_hi:[1,0]
	v_pk_mul_f32 v[88:89], v[88:89], v[242:243] op_sel_hi:[1,0]
	v_pk_mul_f32 v[82:83], v[82:83], v[242:243] op_sel_hi:[1,0]
	v_pk_mul_f32 v[84:85], v[84:85], v[242:243] op_sel_hi:[1,0]
	v_pk_mul_f32 v[144:145], v[86:87], v[186:187]
	v_pk_mul_f32 v[146:147], v[88:89], v[186:187]
	v_pk_mul_f32 v[148:149], v[82:83], v[186:187]
	v_pk_mul_f32 v[150:151], v[84:85], v[186:187]
	v_exp_f32_e32 v144, v144
	v_exp_f32_e32 v145, v145
	v_exp_f32_e32 v146, v146
	v_exp_f32_e32 v147, v147
	v_exp_f32_e32 v148, v148
	v_exp_f32_e32 v149, v149
	v_exp_f32_e32 v150, v150
	v_exp_f32_e32 v151, v151
	s_nop 0
	v_pk_add_f32 v[144:145], v[144:145], v[184:185]
	v_pk_add_f32 v[146:147], v[146:147], v[184:185]
	v_pk_add_f32 v[148:149], v[148:149], v[184:185]
	v_pk_add_f32 v[150:151], v[150:151], v[184:185]
	v_rcp_f32_e32 v144, v144
	v_rcp_f32_e32 v145, v145
	v_rcp_f32_e32 v146, v146
	v_rcp_f32_e32 v147, v147
	v_rcp_f32_e32 v148, v148
	v_rcp_f32_e32 v149, v149
	v_rcp_f32_e32 v150, v150
	v_rcp_f32_e32 v151, v151
	s_nop 0
	v_cvt_pk_bf16_f32 v86, v144, v145
	v_cvt_pk_bf16_f32 v87, v146, v147
	v_cvt_pk_bf16_f32 v88, v148, v149
	v_cvt_pk_bf16_f32 v89, v150, v151
	v_mov_b32_e32 v158, v86
	v_mov_b32_e32 v159, v87
	v_mov_b32_e32 v160, v88
	v_mov_b32_e32 v161, v89
	v_mov_b32_dpp v86, v94 row_shl:8 row_mask:0xf bank_mask:0x3
	v_mov_b32_dpp v87, v95 row_shl:8 row_mask:0xf bank_mask:0x3
	v_mov_b32_dpp v88, v96 row_shl:8 row_mask:0xf bank_mask:0x3
	v_mov_b32_dpp v89, v97 row_shl:8 row_mask:0xf bank_mask:0x3
	v_mov_b32_dpp v94, v158 row_shr:8 row_mask:0xf bank_mask:0xc
	v_mov_b32_dpp v95, v159 row_shr:8 row_mask:0xf bank_mask:0xc
	v_mov_b32_dpp v96, v160 row_shr:8 row_mask:0xf bank_mask:0xc
	v_mov_b32_dpp v97, v161 row_shr:8 row_mask:0xf bank_mask:0xc
	s_mul_i32 s28, s22, 32
	v_lshl_add_u64 v[180:181], s[28:29], 0, v[178:179]
	global_store_dwordx4 v[180:181], v[94:97], off
	s_mul_i32 s28, s22, 40
	v_lshl_add_u64 v[180:181], s[28:29], 0, v[178:179]
	global_store_dwordx4 v[180:181], v[86:89], off
	v_pk_mul_f32 v[78:79], v[78:79], v[242:243] op_sel:[0,1] op_sel_hi:[1,1]
	v_pk_mul_f32 v[80:81], v[80:81], v[242:243] op_sel:[0,1] op_sel_hi:[1,1]
	v_pk_mul_f32 v[74:75], v[74:75], v[242:243] op_sel:[0,1] op_sel_hi:[1,1]
	v_pk_mul_f32 v[76:77], v[76:77], v[242:243] op_sel:[0,1] op_sel_hi:[1,1]
	v_pk_mul_f32 v[144:145], v[78:79], v[186:187]
	v_pk_mul_f32 v[146:147], v[80:81], v[186:187]
	v_pk_mul_f32 v[148:149], v[74:75], v[186:187]
	v_pk_mul_f32 v[150:151], v[76:77], v[186:187]
	v_exp_f32_e32 v144, v144
	v_exp_f32_e32 v145, v145
	v_exp_f32_e32 v146, v146
	v_exp_f32_e32 v147, v147
	v_exp_f32_e32 v148, v148
	v_exp_f32_e32 v149, v149
	v_exp_f32_e32 v150, v150
	v_exp_f32_e32 v151, v151
	s_nop 0
	v_pk_add_f32 v[144:145], v[144:145], v[184:185]
	v_pk_add_f32 v[146:147], v[146:147], v[184:185]
	v_pk_add_f32 v[148:149], v[148:149], v[184:185]
	v_pk_add_f32 v[150:151], v[150:151], v[184:185]
	v_rcp_f32_e32 v144, v144
	v_rcp_f32_e32 v145, v145
	v_rcp_f32_e32 v146, v146
	v_rcp_f32_e32 v147, v147
	v_rcp_f32_e32 v148, v148
	v_rcp_f32_e32 v149, v149
	v_rcp_f32_e32 v150, v150
	v_rcp_f32_e32 v151, v151
	s_nop 0
	v_cvt_pk_bf16_f32 v78, v144, v145
	v_cvt_pk_bf16_f32 v79, v146, v147
	v_cvt_pk_bf16_f32 v80, v148, v149
	v_cvt_pk_bf16_f32 v81, v150, v151
	v_pk_mul_f32 v[70:71], v[70:71], v[242:243] op_sel:[0,1] op_sel_hi:[1,1]
	v_pk_mul_f32 v[72:73], v[72:73], v[242:243] op_sel:[0,1] op_sel_hi:[1,1]
	v_pk_mul_f32 v[66:67], v[66:67], v[242:243] op_sel:[0,1] op_sel_hi:[1,1]
	v_pk_mul_f32 v[68:69], v[68:69], v[242:243] op_sel:[0,1] op_sel_hi:[1,1]
	v_pk_mul_f32 v[144:145], v[70:71], v[186:187]
	v_pk_mul_f32 v[146:147], v[72:73], v[186:187]
	v_pk_mul_f32 v[148:149], v[66:67], v[186:187]
	v_pk_mul_f32 v[150:151], v[68:69], v[186:187]
	v_exp_f32_e32 v144, v144
	v_exp_f32_e32 v145, v145
	v_exp_f32_e32 v146, v146
	v_exp_f32_e32 v147, v147
	v_exp_f32_e32 v148, v148
	v_exp_f32_e32 v149, v149
	v_exp_f32_e32 v150, v150
	v_exp_f32_e32 v151, v151
	s_nop 0
	v_pk_add_f32 v[144:145], v[144:145], v[184:185]
	v_pk_add_f32 v[146:147], v[146:147], v[184:185]
	v_pk_add_f32 v[148:149], v[148:149], v[184:185]
	v_pk_add_f32 v[150:151], v[150:151], v[184:185]
	v_rcp_f32_e32 v144, v144
	v_rcp_f32_e32 v145, v145
	v_rcp_f32_e32 v146, v146
	v_rcp_f32_e32 v147, v147
	v_rcp_f32_e32 v148, v148
	v_rcp_f32_e32 v149, v149
	v_rcp_f32_e32 v150, v150
	v_rcp_f32_e32 v151, v151
	s_nop 0
	v_cvt_pk_bf16_f32 v70, v144, v145
	v_cvt_pk_bf16_f32 v71, v146, v147
	v_cvt_pk_bf16_f32 v72, v148, v149
	v_cvt_pk_bf16_f32 v73, v150, v151
	v_mov_b32_e32 v158, v70
	v_mov_b32_e32 v159, v71
	v_mov_b32_e32 v160, v72
	v_mov_b32_e32 v161, v73
	v_mov_b32_dpp v70, v78 row_shl:8 row_mask:0xf bank_mask:0x3
	v_mov_b32_dpp v71, v79 row_shl:8 row_mask:0xf bank_mask:0x3
	v_mov_b32_dpp v72, v80 row_shl:8 row_mask:0xf bank_mask:0x3
	v_mov_b32_dpp v73, v81 row_shl:8 row_mask:0xf bank_mask:0x3
	v_mov_b32_dpp v78, v158 row_shr:8 row_mask:0xf bank_mask:0xc
	v_mov_b32_dpp v79, v159 row_shr:8 row_mask:0xf bank_mask:0xc
	v_mov_b32_dpp v80, v160 row_shr:8 row_mask:0xf bank_mask:0xc
	v_mov_b32_dpp v81, v161 row_shr:8 row_mask:0xf bank_mask:0xc
	s_mul_i32 s28, s22, 48
	v_lshl_add_u64 v[180:181], s[28:29], 0, v[178:179]
	global_store_dwordx4 v[180:181], v[78:81], off
	s_mul_i32 s28, s22, 56
	v_lshl_add_u64 v[180:181], s[28:29], 0, v[178:179]
	global_store_dwordx4 v[180:181], v[70:73], off
	v_pk_mul_f32 v[62:63], v[62:63], v[244:245] op_sel_hi:[1,0]
	v_pk_mul_f32 v[64:65], v[64:65], v[244:245] op_sel_hi:[1,0]
	v_pk_mul_f32 v[58:59], v[58:59], v[244:245] op_sel_hi:[1,0]
	v_pk_mul_f32 v[60:61], v[60:61], v[244:245] op_sel_hi:[1,0]
	v_pk_mul_f32 v[144:145], v[62:63], v[186:187]
	v_pk_mul_f32 v[146:147], v[64:65], v[186:187]
	v_pk_mul_f32 v[148:149], v[58:59], v[186:187]
	v_pk_mul_f32 v[150:151], v[60:61], v[186:187]
	v_exp_f32_e32 v144, v144
	v_exp_f32_e32 v145, v145
	v_exp_f32_e32 v146, v146
	v_exp_f32_e32 v147, v147
	v_exp_f32_e32 v148, v148
	v_exp_f32_e32 v149, v149
	v_exp_f32_e32 v150, v150
	v_exp_f32_e32 v151, v151
	s_nop 0
	v_pk_add_f32 v[144:145], v[144:145], v[184:185]
	v_pk_add_f32 v[146:147], v[146:147], v[184:185]
	v_pk_add_f32 v[148:149], v[148:149], v[184:185]
	v_pk_add_f32 v[150:151], v[150:151], v[184:185]
	v_rcp_f32_e32 v144, v144
	v_rcp_f32_e32 v145, v145
	v_rcp_f32_e32 v146, v146
	v_rcp_f32_e32 v147, v147
	v_rcp_f32_e32 v148, v148
	v_rcp_f32_e32 v149, v149
	v_rcp_f32_e32 v150, v150
	v_rcp_f32_e32 v151, v151
	s_nop 0
	v_cvt_pk_bf16_f32 v62, v144, v145
	v_cvt_pk_bf16_f32 v63, v146, v147
	v_cvt_pk_bf16_f32 v64, v148, v149
	v_cvt_pk_bf16_f32 v65, v150, v151
	v_pk_mul_f32 v[54:55], v[54:55], v[244:245] op_sel_hi:[1,0]
	v_pk_mul_f32 v[56:57], v[56:57], v[244:245] op_sel_hi:[1,0]
	v_pk_mul_f32 v[50:51], v[50:51], v[244:245] op_sel_hi:[1,0]
	v_pk_mul_f32 v[52:53], v[52:53], v[244:245] op_sel_hi:[1,0]
	v_pk_mul_f32 v[144:145], v[54:55], v[186:187]
	v_pk_mul_f32 v[146:147], v[56:57], v[186:187]
	v_pk_mul_f32 v[148:149], v[50:51], v[186:187]
	v_pk_mul_f32 v[150:151], v[52:53], v[186:187]
	v_exp_f32_e32 v144, v144
	v_exp_f32_e32 v145, v145
	v_exp_f32_e32 v146, v146
	v_exp_f32_e32 v147, v147
	v_exp_f32_e32 v148, v148
	v_exp_f32_e32 v149, v149
	v_exp_f32_e32 v150, v150
	v_exp_f32_e32 v151, v151
	s_nop 0
	v_pk_add_f32 v[144:145], v[144:145], v[184:185]
	v_pk_add_f32 v[146:147], v[146:147], v[184:185]
	v_pk_add_f32 v[148:149], v[148:149], v[184:185]
	v_pk_add_f32 v[150:151], v[150:151], v[184:185]
	v_rcp_f32_e32 v144, v144
	v_rcp_f32_e32 v145, v145
	v_rcp_f32_e32 v146, v146
	v_rcp_f32_e32 v147, v147
	v_rcp_f32_e32 v148, v148
	v_rcp_f32_e32 v149, v149
	v_rcp_f32_e32 v150, v150
	v_rcp_f32_e32 v151, v151
	s_nop 0
	v_cvt_pk_bf16_f32 v54, v144, v145
	v_cvt_pk_bf16_f32 v55, v146, v147
	v_cvt_pk_bf16_f32 v56, v148, v149
	v_cvt_pk_bf16_f32 v57, v150, v151
	v_mov_b32_e32 v158, v54
	v_mov_b32_e32 v159, v55
	v_mov_b32_e32 v160, v56
	v_mov_b32_e32 v161, v57
	v_mov_b32_dpp v54, v62 row_shl:8 row_mask:0xf bank_mask:0x3
	v_mov_b32_dpp v55, v63 row_shl:8 row_mask:0xf bank_mask:0x3
	v_mov_b32_dpp v56, v64 row_shl:8 row_mask:0xf bank_mask:0x3
	v_mov_b32_dpp v57, v65 row_shl:8 row_mask:0xf bank_mask:0x3
	v_mov_b32_dpp v62, v158 row_shr:8 row_mask:0xf bank_mask:0xc
	v_mov_b32_dpp v63, v159 row_shr:8 row_mask:0xf bank_mask:0xc
	v_mov_b32_dpp v64, v160 row_shr:8 row_mask:0xf bank_mask:0xc
	v_mov_b32_dpp v65, v161 row_shr:8 row_mask:0xf bank_mask:0xc
	s_mul_i32 s28, s22, 128
	v_lshl_add_u64 v[180:181], s[28:29], 0, v[178:179]
	global_store_dwordx4 v[180:181], v[62:65], off
	s_mul_i32 s28, s22, 136
	v_lshl_add_u64 v[180:181], s[28:29], 0, v[178:179]
	global_store_dwordx4 v[180:181], v[54:57], off
	v_pk_mul_f32 v[46:47], v[46:47], v[244:245] op_sel:[0,1] op_sel_hi:[1,1]
	v_pk_mul_f32 v[48:49], v[48:49], v[244:245] op_sel:[0,1] op_sel_hi:[1,1]
	v_pk_mul_f32 v[42:43], v[42:43], v[244:245] op_sel:[0,1] op_sel_hi:[1,1]
	v_pk_mul_f32 v[44:45], v[44:45], v[244:245] op_sel:[0,1] op_sel_hi:[1,1]
	v_pk_mul_f32 v[144:145], v[46:47], v[186:187]
	v_pk_mul_f32 v[146:147], v[48:49], v[186:187]
	v_pk_mul_f32 v[148:149], v[42:43], v[186:187]
	v_pk_mul_f32 v[150:151], v[44:45], v[186:187]
	v_exp_f32_e32 v144, v144
	v_exp_f32_e32 v145, v145
	v_exp_f32_e32 v146, v146
	v_exp_f32_e32 v147, v147
	v_exp_f32_e32 v148, v148
	v_exp_f32_e32 v149, v149
	v_exp_f32_e32 v150, v150
	v_exp_f32_e32 v151, v151
	s_nop 0
	v_pk_add_f32 v[144:145], v[144:145], v[184:185]
	v_pk_add_f32 v[146:147], v[146:147], v[184:185]
	v_pk_add_f32 v[148:149], v[148:149], v[184:185]
	v_pk_add_f32 v[150:151], v[150:151], v[184:185]
	v_rcp_f32_e32 v144, v144
	v_rcp_f32_e32 v145, v145
	v_rcp_f32_e32 v146, v146
	v_rcp_f32_e32 v147, v147
	v_rcp_f32_e32 v148, v148
	v_rcp_f32_e32 v149, v149
	v_rcp_f32_e32 v150, v150
	v_rcp_f32_e32 v151, v151
	s_nop 0
	v_cvt_pk_bf16_f32 v46, v144, v145
	v_cvt_pk_bf16_f32 v47, v146, v147
	v_cvt_pk_bf16_f32 v48, v148, v149
	v_cvt_pk_bf16_f32 v49, v150, v151
	v_pk_mul_f32 v[38:39], v[38:39], v[244:245] op_sel:[0,1] op_sel_hi:[1,1]
	v_pk_mul_f32 v[40:41], v[40:41], v[244:245] op_sel:[0,1] op_sel_hi:[1,1]
	v_pk_mul_f32 v[34:35], v[34:35], v[244:245] op_sel:[0,1] op_sel_hi:[1,1]
	v_pk_mul_f32 v[36:37], v[36:37], v[244:245] op_sel:[0,1] op_sel_hi:[1,1]
	v_pk_mul_f32 v[144:145], v[38:39], v[186:187]
	v_pk_mul_f32 v[146:147], v[40:41], v[186:187]
	v_pk_mul_f32 v[148:149], v[34:35], v[186:187]
	v_pk_mul_f32 v[150:151], v[36:37], v[186:187]
	v_exp_f32_e32 v144, v144
	v_exp_f32_e32 v145, v145
	v_exp_f32_e32 v146, v146
	v_exp_f32_e32 v147, v147
	v_exp_f32_e32 v148, v148
	v_exp_f32_e32 v149, v149
	v_exp_f32_e32 v150, v150
	v_exp_f32_e32 v151, v151
	s_nop 0
	v_pk_add_f32 v[144:145], v[144:145], v[184:185]
	v_pk_add_f32 v[146:147], v[146:147], v[184:185]
	v_pk_add_f32 v[148:149], v[148:149], v[184:185]
	v_pk_add_f32 v[150:151], v[150:151], v[184:185]
	v_rcp_f32_e32 v144, v144
	v_rcp_f32_e32 v145, v145
	v_rcp_f32_e32 v146, v146
	v_rcp_f32_e32 v147, v147
	v_rcp_f32_e32 v148, v148
	v_rcp_f32_e32 v149, v149
	v_rcp_f32_e32 v150, v150
	v_rcp_f32_e32 v151, v151
	s_nop 0
	v_cvt_pk_bf16_f32 v38, v144, v145
	v_cvt_pk_bf16_f32 v39, v146, v147
	v_cvt_pk_bf16_f32 v40, v148, v149
	v_cvt_pk_bf16_f32 v41, v150, v151
	v_mov_b32_e32 v158, v38
	v_mov_b32_e32 v159, v39
	v_mov_b32_e32 v160, v40
	v_mov_b32_e32 v161, v41
	v_mov_b32_dpp v38, v46 row_shl:8 row_mask:0xf bank_mask:0x3
	v_mov_b32_dpp v39, v47 row_shl:8 row_mask:0xf bank_mask:0x3
	v_mov_b32_dpp v40, v48 row_shl:8 row_mask:0xf bank_mask:0x3
	v_mov_b32_dpp v41, v49 row_shl:8 row_mask:0xf bank_mask:0x3
	v_mov_b32_dpp v46, v158 row_shr:8 row_mask:0xf bank_mask:0xc
	v_mov_b32_dpp v47, v159 row_shr:8 row_mask:0xf bank_mask:0xc
	v_mov_b32_dpp v48, v160 row_shr:8 row_mask:0xf bank_mask:0xc
	v_mov_b32_dpp v49, v161 row_shr:8 row_mask:0xf bank_mask:0xc
	s_mul_i32 s28, s22, 144
	v_lshl_add_u64 v[180:181], s[28:29], 0, v[178:179]
	global_store_dwordx4 v[180:181], v[46:49], off
	s_mul_i32 s28, s22, 152
	v_lshl_add_u64 v[180:181], s[28:29], 0, v[178:179]
	global_store_dwordx4 v[180:181], v[38:41], off
	v_pk_mul_f32 v[30:31], v[30:31], v[246:247] op_sel_hi:[1,0]
	v_pk_mul_f32 v[32:33], v[32:33], v[246:247] op_sel_hi:[1,0]
	v_pk_mul_f32 v[26:27], v[26:27], v[246:247] op_sel_hi:[1,0]
	v_pk_mul_f32 v[28:29], v[28:29], v[246:247] op_sel_hi:[1,0]
	v_pk_mul_f32 v[144:145], v[30:31], v[186:187]
	v_pk_mul_f32 v[146:147], v[32:33], v[186:187]
	v_pk_mul_f32 v[148:149], v[26:27], v[186:187]
	v_pk_mul_f32 v[150:151], v[28:29], v[186:187]
	v_exp_f32_e32 v144, v144
	v_exp_f32_e32 v145, v145
	v_exp_f32_e32 v146, v146
	v_exp_f32_e32 v147, v147
	v_exp_f32_e32 v148, v148
	v_exp_f32_e32 v149, v149
	v_exp_f32_e32 v150, v150
	v_exp_f32_e32 v151, v151
	s_nop 0
	v_pk_add_f32 v[144:145], v[144:145], v[184:185]
	v_pk_add_f32 v[146:147], v[146:147], v[184:185]
	v_pk_add_f32 v[148:149], v[148:149], v[184:185]
	v_pk_add_f32 v[150:151], v[150:151], v[184:185]
	v_rcp_f32_e32 v144, v144
	v_rcp_f32_e32 v145, v145
	v_rcp_f32_e32 v146, v146
	v_rcp_f32_e32 v147, v147
	v_rcp_f32_e32 v148, v148
	v_rcp_f32_e32 v149, v149
	v_rcp_f32_e32 v150, v150
	v_rcp_f32_e32 v151, v151
	s_nop 0
	v_cvt_pk_bf16_f32 v30, v144, v145
	v_cvt_pk_bf16_f32 v31, v146, v147
	v_cvt_pk_bf16_f32 v32, v148, v149
	v_cvt_pk_bf16_f32 v33, v150, v151
	v_pk_mul_f32 v[22:23], v[22:23], v[246:247] op_sel_hi:[1,0]
	v_pk_mul_f32 v[24:25], v[24:25], v[246:247] op_sel_hi:[1,0]
	v_pk_mul_f32 v[18:19], v[18:19], v[246:247] op_sel_hi:[1,0]
	v_pk_mul_f32 v[20:21], v[20:21], v[246:247] op_sel_hi:[1,0]
	v_pk_mul_f32 v[144:145], v[22:23], v[186:187]
	v_pk_mul_f32 v[146:147], v[24:25], v[186:187]
	v_pk_mul_f32 v[148:149], v[18:19], v[186:187]
	v_pk_mul_f32 v[150:151], v[20:21], v[186:187]
	v_exp_f32_e32 v144, v144
	v_exp_f32_e32 v145, v145
	v_exp_f32_e32 v146, v146
	v_exp_f32_e32 v147, v147
	v_exp_f32_e32 v148, v148
	v_exp_f32_e32 v149, v149
	v_exp_f32_e32 v150, v150
	v_exp_f32_e32 v151, v151
	s_nop 0
	v_pk_add_f32 v[144:145], v[144:145], v[184:185]
	v_pk_add_f32 v[146:147], v[146:147], v[184:185]
	v_pk_add_f32 v[148:149], v[148:149], v[184:185]
	v_pk_add_f32 v[150:151], v[150:151], v[184:185]
	v_rcp_f32_e32 v144, v144
	v_rcp_f32_e32 v145, v145
	v_rcp_f32_e32 v146, v146
	v_rcp_f32_e32 v147, v147
	v_rcp_f32_e32 v148, v148
	v_rcp_f32_e32 v149, v149
	v_rcp_f32_e32 v150, v150
	v_rcp_f32_e32 v151, v151
	s_nop 0
	v_cvt_pk_bf16_f32 v22, v144, v145
	v_cvt_pk_bf16_f32 v23, v146, v147
	v_cvt_pk_bf16_f32 v24, v148, v149
	v_cvt_pk_bf16_f32 v25, v150, v151
	v_mov_b32_e32 v158, v22
	v_mov_b32_e32 v159, v23
	v_mov_b32_e32 v160, v24
	v_mov_b32_e32 v161, v25
	v_mov_b32_dpp v22, v30 row_shl:8 row_mask:0xf bank_mask:0x3
	v_mov_b32_dpp v23, v31 row_shl:8 row_mask:0xf bank_mask:0x3
	v_mov_b32_dpp v24, v32 row_shl:8 row_mask:0xf bank_mask:0x3
	v_mov_b32_dpp v25, v33 row_shl:8 row_mask:0xf bank_mask:0x3
	v_mov_b32_dpp v30, v158 row_shr:8 row_mask:0xf bank_mask:0xc
	v_mov_b32_dpp v31, v159 row_shr:8 row_mask:0xf bank_mask:0xc
	v_mov_b32_dpp v32, v160 row_shr:8 row_mask:0xf bank_mask:0xc
	v_mov_b32_dpp v33, v161 row_shr:8 row_mask:0xf bank_mask:0xc
	s_mul_i32 s28, s22, 160
	v_lshl_add_u64 v[180:181], s[28:29], 0, v[178:179]
	global_store_dwordx4 v[180:181], v[30:33], off
	s_mul_i32 s28, s22, 168
	v_lshl_add_u64 v[180:181], s[28:29], 0, v[178:179]
	global_store_dwordx4 v[180:181], v[22:25], off
	v_pk_mul_f32 v[14:15], v[14:15], v[246:247] op_sel:[0,1] op_sel_hi:[1,1]
	v_pk_mul_f32 v[16:17], v[16:17], v[246:247] op_sel:[0,1] op_sel_hi:[1,1]
	v_pk_mul_f32 v[10:11], v[10:11], v[246:247] op_sel:[0,1] op_sel_hi:[1,1]
	v_pk_mul_f32 v[12:13], v[12:13], v[246:247] op_sel:[0,1] op_sel_hi:[1,1]
	v_pk_mul_f32 v[144:145], v[14:15], v[186:187]
	v_pk_mul_f32 v[146:147], v[16:17], v[186:187]
	v_pk_mul_f32 v[148:149], v[10:11], v[186:187]
	v_pk_mul_f32 v[150:151], v[12:13], v[186:187]
	v_exp_f32_e32 v144, v144
	v_exp_f32_e32 v145, v145
	v_exp_f32_e32 v146, v146
	v_exp_f32_e32 v147, v147
	v_exp_f32_e32 v148, v148
	v_exp_f32_e32 v149, v149
	v_exp_f32_e32 v150, v150
	v_exp_f32_e32 v151, v151
	s_nop 0
	v_pk_add_f32 v[144:145], v[144:145], v[184:185]
	v_pk_add_f32 v[146:147], v[146:147], v[184:185]
	v_pk_add_f32 v[148:149], v[148:149], v[184:185]
	v_pk_add_f32 v[150:151], v[150:151], v[184:185]
	v_rcp_f32_e32 v144, v144
	v_rcp_f32_e32 v145, v145
	v_rcp_f32_e32 v146, v146
	v_rcp_f32_e32 v147, v147
	v_rcp_f32_e32 v148, v148
	v_rcp_f32_e32 v149, v149
	v_rcp_f32_e32 v150, v150
	v_rcp_f32_e32 v151, v151
	s_nop 0
	v_cvt_pk_bf16_f32 v14, v144, v145
	v_cvt_pk_bf16_f32 v15, v146, v147
	v_cvt_pk_bf16_f32 v16, v148, v149
	v_cvt_pk_bf16_f32 v17, v150, v151
	v_pk_mul_f32 v[6:7], v[6:7], v[246:247] op_sel:[0,1] op_sel_hi:[1,1]
	v_pk_mul_f32 v[8:9], v[8:9], v[246:247] op_sel:[0,1] op_sel_hi:[1,1]
	v_pk_mul_f32 v[2:3], v[2:3], v[246:247] op_sel:[0,1] op_sel_hi:[1,1]
	v_pk_mul_f32 v[4:5], v[4:5], v[246:247] op_sel:[0,1] op_sel_hi:[1,1]
	v_pk_mul_f32 v[144:145], v[6:7], v[186:187]
	v_pk_mul_f32 v[146:147], v[8:9], v[186:187]
	v_pk_mul_f32 v[148:149], v[2:3], v[186:187]
	v_pk_mul_f32 v[150:151], v[4:5], v[186:187]
	v_exp_f32_e32 v144, v144
	v_exp_f32_e32 v145, v145
	v_exp_f32_e32 v146, v146
	v_exp_f32_e32 v147, v147
	v_exp_f32_e32 v148, v148
	v_exp_f32_e32 v149, v149
	v_exp_f32_e32 v150, v150
	v_exp_f32_e32 v151, v151
	s_nop 0
	v_pk_add_f32 v[144:145], v[144:145], v[184:185]
	v_pk_add_f32 v[146:147], v[146:147], v[184:185]
	v_pk_add_f32 v[148:149], v[148:149], v[184:185]
	v_pk_add_f32 v[150:151], v[150:151], v[184:185]
	v_rcp_f32_e32 v144, v144
	v_rcp_f32_e32 v145, v145
	v_rcp_f32_e32 v146, v146
	v_rcp_f32_e32 v147, v147
	v_rcp_f32_e32 v148, v148
	v_rcp_f32_e32 v149, v149
	v_rcp_f32_e32 v150, v150
	v_rcp_f32_e32 v151, v151
	s_nop 0
	v_cvt_pk_bf16_f32 v6, v144, v145
	v_cvt_pk_bf16_f32 v7, v146, v147
	v_cvt_pk_bf16_f32 v8, v148, v149
	v_cvt_pk_bf16_f32 v9, v150, v151
	v_mov_b32_e32 v158, v6
	v_mov_b32_e32 v159, v7
	v_mov_b32_e32 v160, v8
	v_mov_b32_e32 v161, v9
	v_mov_b32_dpp v6, v14 row_shl:8 row_mask:0xf bank_mask:0x3
	v_mov_b32_dpp v7, v15 row_shl:8 row_mask:0xf bank_mask:0x3
	v_mov_b32_dpp v8, v16 row_shl:8 row_mask:0xf bank_mask:0x3
	v_mov_b32_dpp v9, v17 row_shl:8 row_mask:0xf bank_mask:0x3
	v_mov_b32_dpp v14, v158 row_shr:8 row_mask:0xf bank_mask:0xc
	v_mov_b32_dpp v15, v159 row_shr:8 row_mask:0xf bank_mask:0xc
	v_mov_b32_dpp v16, v160 row_shr:8 row_mask:0xf bank_mask:0xc
	v_mov_b32_dpp v17, v161 row_shr:8 row_mask:0xf bank_mask:0xc
	s_mul_i32 s28, s22, 176
	v_lshl_add_u64 v[180:181], s[28:29], 0, v[178:179]
	global_store_dwordx4 v[180:181], v[14:17], off
	s_mul_i32 s28, s22, 184
	v_lshl_add_u64 v[180:181], s[28:29], 0, v[178:179]
	global_store_dwordx4 v[180:181], v[6:9], off

.LBB0_2800:
	s_andn2_b64 vcc, exec, s[16:17]
	s_waitcnt vmcnt(0)
	v_lshl_add_u32 v248, s67, 8, v139
	v_ashrrev_i32_e32 v249, 31, v248
	v_lshl_add_u64 v[250:251], v[248:249], 2, s[14:15]
	global_load_dword v240, v[250:251], off
	global_load_dword v241, v[250:251], off offset:64
	global_load_dword v242, v[250:251], off offset:128
	global_load_dword v243, v[250:251], off offset:192
	global_load_dword v244, v[250:251], off offset:512
	global_load_dword v245, v[250:251], off offset:576
	global_load_dword v246, v[250:251], off offset:640
	global_load_dword v247, v[250:251], off offset:704
	s_cbranch_vccnz .LBB0_2803
	s_add_u32 s69, s22, s38
	s_addc_u32 s70, s23, 0
	s_add_u32 s71, s0, s8
	s_addc_u32 s72, s1, s9
	s_add_u32 s73, s20, s8
	s_addc_u32 s74, s21, s9
	s_mov_b32 s75, 0
	v_mov_b32_e32 v2, 0
	v_mov_b32_e32 v3, 0
	v_mov_b32_e32 v4, 0
	v_mov_b32_e32 v5, 0
	s_nop 1
	v_mfma_f32_32x32x16_bf16 v[18:33], v[2:5], v[2:5], 0
	v_mfma_f32_32x32x16_bf16 v[34:49], v[2:5], v[2:5], 0
	v_mfma_f32_32x32x16_bf16 v[50:65], v[2:5], v[2:5], 0
	v_mfma_f32_32x32x16_bf16 v[66:81], v[2:5], v[2:5], 0
	v_mfma_f32_32x32x16_bf16 v[82:97], v[2:5], v[2:5], 0
	v_mfma_f32_32x32x16_bf16 v[98:113], v[2:5], v[2:5], 0
	v_mfma_f32_32x32x16_bf16 v[114:129], v[2:5], v[2:5], 0
	v_mfma_f32_16x16x32_bf16 v[6:9], v[2:5], v[2:5], 0
	v_mfma_f32_16x16x32_bf16 v[10:13], v[2:5], v[2:5], 0
	v_mfma_f32_16x16x32_bf16 v[14:17], v[2:5], v[2:5], 0

.LBB0_2803:
	v_lshl_add_u32 v146, s67, 8, v139
	v_ashrrev_i32_e32 v147, 31, v146
	s_and_b64 vcc, exec, s[18:19]
	s_cbranch_vccz .LBB0_2805
	s_barrier
.LBB0_2805:
	s_mul_hi_i32 s22, s68, 0x2e8ba2e9
	s_lshr_b32 s23, s22, 31
	s_lshr_b32 s22, s22, 2
	s_add_i32 s22, s22, s23
	s_mul_i32 s22, s22, 22
	s_sub_i32 s22, s68, s22
	v_lshl_or_b32 v150, s22, 7, v143
	v_lshlrev_b32_e32 v150, 1, v150
	v_mov_b32_e32 v151, 0
	s_mov_b32 s24, 0x1600
	v_mov_b64_e32 v[154:155], s[12:13]
	v_mad_u64_u32 v[152:153], s[22:23], v146, s24, v[154:155]
	v_lshl_add_u64 v[152:153], v[152:153], 0, v[150:151]
	v_mov_b32_e32 v158, 1.0
	v_mov_b32_e32 v159, 1.0
	v_mov_b32_e32 v160, 0xbfb8aa3b
	v_mov_b32_e32 v161, 0xbfb8aa3b
	s_mov_b32 s23, 0
	s_waitcnt vmcnt(8)
	v_pk_mul_f32 v[122:123], v[122:123], v[240:241] op_sel_hi:[1,0]
	v_pk_mul_f32 v[124:125], v[124:125], v[240:241] op_sel_hi:[1,0]
	v_pk_mul_f32 v[114:115], v[114:115], v[240:241] op_sel_hi:[1,0]
	v_pk_mul_f32 v[116:117], v[116:117], v[240:241] op_sel_hi:[1,0]
	v_pk_mul_f32 v[126:127], v[126:127], v[240:241] op_sel_hi:[1,0]
	v_pk_mul_f32 v[128:129], v[128:129], v[240:241] op_sel_hi:[1,0]
	v_pk_mul_f32 v[118:119], v[118:119], v[240:241] op_sel_hi:[1,0]
	v_pk_mul_f32 v[120:121], v[120:121], v[240:241] op_sel_hi:[1,0]
	v_pk_mul_f32 v[172:173], v[122:123], v[160:161]
	v_pk_mul_f32 v[174:175], v[124:125], v[160:161]
	v_pk_mul_f32 v[176:177], v[114:115], v[160:161]
	v_pk_mul_f32 v[178:179], v[116:117], v[160:161]
	v_exp_f32_e32 v172, v172
	v_exp_f32_e32 v173, v173
	v_exp_f32_e32 v174, v174
	v_exp_f32_e32 v175, v175
	v_exp_f32_e32 v176, v176
	v_exp_f32_e32 v177, v177
	v_exp_f32_e32 v178, v178
	v_exp_f32_e32 v179, v179
	s_mov_b32 s22, 0x0
	v_lshl_add_u64 v[154:155], s[22:23], 0, v[152:153]
	v_pk_add_f32 v[172:173], v[172:173], v[158:159]
	v_pk_add_f32 v[174:175], v[174:175], v[158:159]
	v_pk_add_f32 v[176:177], v[176:177], v[158:159]
	v_pk_add_f32 v[178:179], v[178:179], v[158:159]
	v_rcp_f32_e32 v172, v172
	v_rcp_f32_e32 v173, v173
	v_rcp_f32_e32 v174, v174
	v_rcp_f32_e32 v175, v175
	v_rcp_f32_e32 v176, v176
	v_rcp_f32_e32 v177, v177
	v_rcp_f32_e32 v178, v178
	v_rcp_f32_e32 v179, v179
	s_nop 0
	v_pk_mul_f32 v[122:123], v[122:123], v[172:173]
	v_pk_mul_f32 v[124:125], v[124:125], v[174:175]
	v_pk_mul_f32 v[114:115], v[114:115], v[176:177]
	v_pk_mul_f32 v[116:117], v[116:117], v[178:179]
	v_pk_mul_f32 v[122:123], v[126:127], v[122:123]
	v_pk_mul_f32 v[124:125], v[128:129], v[124:125]
	v_pk_mul_f32 v[114:115], v[118:119], v[114:115]
	v_pk_mul_f32 v[116:117], v[120:121], v[116:117]
	v_cvt_pk_bf16_f32 v122, v122, v123
	v_cvt_pk_bf16_f32 v123, v124, v125
	v_cvt_pk_bf16_f32 v124, v114, v115
	v_cvt_pk_bf16_f32 v125, v116, v117
	global_store_dwordx4 v[154:155], v[122:125], off
	v_pk_mul_f32 v[106:107], v[106:107], v[240:241] op_sel:[0,1] op_sel_hi:[1,1]
	v_pk_mul_f32 v[108:109], v[108:109], v[240:241] op_sel:[0,1] op_sel_hi:[1,1]
	v_pk_mul_f32 v[98:99], v[98:99], v[240:241] op_sel:[0,1] op_sel_hi:[1,1]
	v_pk_mul_f32 v[100:101], v[100:101], v[240:241] op_sel:[0,1] op_sel_hi:[1,1]
	v_pk_mul_f32 v[110:111], v[110:111], v[240:241] op_sel:[0,1] op_sel_hi:[1,1]
	v_pk_mul_f32 v[112:113], v[112:113], v[240:241] op_sel:[0,1] op_sel_hi:[1,1]
	v_pk_mul_f32 v[102:103], v[102:103], v[240:241] op_sel:[0,1] op_sel_hi:[1,1]
	v_pk_mul_f32 v[104:105], v[104:105], v[240:241] op_sel:[0,1] op_sel_hi:[1,1]
	v_pk_mul_f32 v[172:173], v[106:107], v[160:161]
	v_pk_mul_f32 v[174:175], v[108:109], v[160:161]
	v_pk_mul_f32 v[176:177], v[98:99], v[160:161]
	v_pk_mul_f32 v[178:179], v[100:101], v[160:161]
	v_exp_f32_e32 v172, v172
	v_exp_f32_e32 v173, v173
	v_exp_f32_e32 v174, v174
	v_exp_f32_e32 v175, v175
	v_exp_f32_e32 v176, v176
	v_exp_f32_e32 v177, v177
	v_exp_f32_e32 v178, v178
	v_exp_f32_e32 v179, v179
	s_mov_b32 s22, 0x16000
	v_lshl_add_u64 v[156:157], s[22:23], 0, v[152:153]
	v_pk_add_f32 v[172:173], v[172:173], v[158:159]
	v_pk_add_f32 v[174:175], v[174:175], v[158:159]
	v_pk_add_f32 v[176:177], v[176:177], v[158:159]
	v_pk_add_f32 v[178:179], v[178:179], v[158:159]
	v_rcp_f32_e32 v172, v172
	v_rcp_f32_e32 v173, v173
	v_rcp_f32_e32 v174, v174
	v_rcp_f32_e32 v175, v175
	v_rcp_f32_e32 v176, v176
	v_rcp_f32_e32 v177, v177
	v_rcp_f32_e32 v178, v178
	v_rcp_f32_e32 v179, v179
	s_nop 0
	v_pk_mul_f32 v[106:107], v[106:107], v[172:173]
	v_pk_mul_f32 v[108:109], v[108:109], v[174:175]
	v_pk_mul_f32 v[98:99], v[98:99], v[176:177]
	v_pk_mul_f32 v[100:101], v[100:101], v[178:179]
	v_pk_mul_f32 v[106:107], v[110:111], v[106:107]
	v_pk_mul_f32 v[108:109], v[112:113], v[108:109]
	v_pk_mul_f32 v[98:99], v[102:103], v[98:99]
	v_pk_mul_f32 v[100:101], v[104:105], v[100:101]
	v_cvt_pk_bf16_f32 v106, v106, v107
	v_cvt_pk_bf16_f32 v107, v108, v109
	v_cvt_pk_bf16_f32 v108, v98, v99
	v_cvt_pk_bf16_f32 v109, v100, v101
	global_store_dwordx4 v[156:157], v[106:109], off
	v_pk_mul_f32 v[90:91], v[90:91], v[242:243] op_sel_hi:[1,0]
	v_pk_mul_f32 v[92:93], v[92:93], v[242:243] op_sel_hi:[1,0]
	v_pk_mul_f32 v[82:83], v[82:83], v[242:243] op_sel_hi:[1,0]
	v_pk_mul_f32 v[84:85], v[84:85], v[242:243] op_sel_hi:[1,0]
	v_pk_mul_f32 v[94:95], v[94:95], v[242:243] op_sel_hi:[1,0]
	v_pk_mul_f32 v[96:97], v[96:97], v[242:243] op_sel_hi:[1,0]
	v_pk_mul_f32 v[86:87], v[86:87], v[242:243] op_sel_hi:[1,0]
	v_pk_mul_f32 v[88:89], v[88:89], v[242:243] op_sel_hi:[1,0]
	v_pk_mul_f32 v[172:173], v[90:91], v[160:161]
	v_pk_mul_f32 v[174:175], v[92:93], v[160:161]
	v_pk_mul_f32 v[176:177], v[82:83], v[160:161]
	v_pk_mul_f32 v[178:179], v[84:85], v[160:161]
	v_exp_f32_e32 v172, v172
	v_exp_f32_e32 v173, v173
	v_exp_f32_e32 v174, v174
	v_exp_f32_e32 v175, v175
	v_exp_f32_e32 v176, v176
	v_exp_f32_e32 v177, v177
	v_exp_f32_e32 v178, v178
	v_exp_f32_e32 v179, v179
	s_mov_b32 s22, 0x2c000
	v_lshl_add_u64 v[154:155], s[22:23], 0, v[152:153]
	v_pk_add_f32 v[172:173], v[172:173], v[158:159]
	v_pk_add_f32 v[174:175], v[174:175], v[158:159]
	v_pk_add_f32 v[176:177], v[176:177], v[158:159]
	v_pk_add_f32 v[178:179], v[178:179], v[158:159]
	v_rcp_f32_e32 v172, v172
	v_rcp_f32_e32 v173, v173
	v_rcp_f32_e32 v174, v174
	v_rcp_f32_e32 v175, v175
	v_rcp_f32_e32 v176, v176
	v_rcp_f32_e32 v177, v177
	v_rcp_f32_e32 v178, v178
	v_rcp_f32_e32 v179, v179
	s_nop 0
	v_pk_mul_f32 v[90:91], v[90:91], v[172:173]
	v_pk_mul_f32 v[92:93], v[92:93], v[174:175]
	v_pk_mul_f32 v[82:83], v[82:83], v[176:177]
	v_pk_mul_f32 v[84:85], v[84:85], v[178:179]
	v_pk_mul_f32 v[90:91], v[94:95], v[90:91]
	v_pk_mul_f32 v[92:93], v[96:97], v[92:93]
	v_pk_mul_f32 v[82:83], v[86:87], v[82:83]
	v_pk_mul_f32 v[84:85], v[88:89], v[84:85]
	v_cvt_pk_bf16_f32 v90, v90, v91
	v_cvt_pk_bf16_f32 v91, v92, v93
	v_cvt_pk_bf16_f32 v92, v82, v83
	v_cvt_pk_bf16_f32 v93, v84, v85
	global_store_dwordx4 v[154:155], v[90:93], off
	v_pk_mul_f32 v[74:75], v[74:75], v[242:243] op_sel:[0,1] op_sel_hi:[1,1]
	v_pk_mul_f32 v[76:77], v[76:77], v[242:243] op_sel:[0,1] op_sel_hi:[1,1]
	v_pk_mul_f32 v[66:67], v[66:67], v[242:243] op_sel:[0,1] op_sel_hi:[1,1]
	v_pk_mul_f32 v[68:69], v[68:69], v[242:243] op_sel:[0,1] op_sel_hi:[1,1]
	v_pk_mul_f32 v[78:79], v[78:79], v[242:243] op_sel:[0,1] op_sel_hi:[1,1]
	v_pk_mul_f32 v[80:81], v[80:81], v[242:243] op_sel:[0,1] op_sel_hi:[1,1]
	v_pk_mul_f32 v[70:71], v[70:71], v[242:243] op_sel:[0,1] op_sel_hi:[1,1]
	v_pk_mul_f32 v[72:73], v[72:73], v[242:243] op_sel:[0,1] op_sel_hi:[1,1]
	v_pk_mul_f32 v[172:173], v[74:75], v[160:161]
	v_pk_mul_f32 v[174:175], v[76:77], v[160:161]
	v_pk_mul_f32 v[176:177], v[66:67], v[160:161]
	v_pk_mul_f32 v[178:179], v[68:69], v[160:161]
	v_exp_f32_e32 v172, v172
	v_exp_f32_e32 v173, v173
	v_exp_f32_e32 v174, v174
	v_exp_f32_e32 v175, v175
	v_exp_f32_e32 v176, v176
	v_exp_f32_e32 v177, v177
	v_exp_f32_e32 v178, v178
	v_exp_f32_e32 v179, v179
	s_mov_b32 s22, 0x42000
	v_lshl_add_u64 v[156:157], s[22:23], 0, v[152:153]
	v_pk_add_f32 v[172:173], v[172:173], v[158:159]
	v_pk_add_f32 v[174:175], v[174:175], v[158:159]
	v_pk_add_f32 v[176:177], v[176:177], v[158:159]
	v_pk_add_f32 v[178:179], v[178:179], v[158:159]
	v_rcp_f32_e32 v172, v172
	v_rcp_f32_e32 v173, v173
	v_rcp_f32_e32 v174, v174
	v_rcp_f32_e32 v175, v175
	v_rcp_f32_e32 v176, v176
	v_rcp_f32_e32 v177, v177
	v_rcp_f32_e32 v178, v178
	v_rcp_f32_e32 v179, v179
	s_nop 0
	v_pk_mul_f32 v[74:75], v[74:75], v[172:173]
	v_pk_mul_f32 v[76:77], v[76:77], v[174:175]
	v_pk_mul_f32 v[66:67], v[66:67], v[176:177]
	v_pk_mul_f32 v[68:69], v[68:69], v[178:179]
	v_pk_mul_f32 v[74:75], v[78:79], v[74:75]
	v_pk_mul_f32 v[76:77], v[80:81], v[76:77]
	v_pk_mul_f32 v[66:67], v[70:71], v[66:67]
	v_pk_mul_f32 v[68:69], v[72:73], v[68:69]
	v_cvt_pk_bf16_f32 v74, v74, v75
	v_cvt_pk_bf16_f32 v75, v76, v77
	v_cvt_pk_bf16_f32 v76, v66, v67
	v_cvt_pk_bf16_f32 v77, v68, v69
	global_store_dwordx4 v[156:157], v[74:77], off
	v_pk_mul_f32 v[58:59], v[58:59], v[244:245] op_sel_hi:[1,0]
	v_pk_mul_f32 v[60:61], v[60:61], v[244:245] op_sel_hi:[1,0]
	v_pk_mul_f32 v[50:51], v[50:51], v[244:245] op_sel_hi:[1,0]
	v_pk_mul_f32 v[52:53], v[52:53], v[244:245] op_sel_hi:[1,0]
	v_pk_mul_f32 v[62:63], v[62:63], v[244:245] op_sel_hi:[1,0]
	v_pk_mul_f32 v[64:65], v[64:65], v[244:245] op_sel_hi:[1,0]
	v_pk_mul_f32 v[54:55], v[54:55], v[244:245] op_sel_hi:[1,0]
	v_pk_mul_f32 v[56:57], v[56:57], v[244:245] op_sel_hi:[1,0]
	v_pk_mul_f32 v[172:173], v[58:59], v[160:161]
	v_pk_mul_f32 v[174:175], v[60:61], v[160:161]
	v_pk_mul_f32 v[176:177], v[50:51], v[160:161]
	v_pk_mul_f32 v[178:179], v[52:53], v[160:161]
	v_exp_f32_e32 v172, v172
	v_exp_f32_e32 v173, v173
	v_exp_f32_e32 v174, v174
	v_exp_f32_e32 v175, v175
	v_exp_f32_e32 v176, v176
	v_exp_f32_e32 v177, v177
	v_exp_f32_e32 v178, v178
	v_exp_f32_e32 v179, v179
	s_mov_b32 s22, 0xb0000
	v_lshl_add_u64 v[154:155], s[22:23], 0, v[152:153]
	v_pk_add_f32 v[172:173], v[172:173], v[158:159]
	v_pk_add_f32 v[174:175], v[174:175], v[158:159]
	v_pk_add_f32 v[176:177], v[176:177], v[158:159]
	v_pk_add_f32 v[178:179], v[178:179], v[158:159]
	v_rcp_f32_e32 v172, v172
	v_rcp_f32_e32 v173, v173
	v_rcp_f32_e32 v174, v174
	v_rcp_f32_e32 v175, v175
	v_rcp_f32_e32 v176, v176
	v_rcp_f32_e32 v177, v177
	v_rcp_f32_e32 v178, v178
	v_rcp_f32_e32 v179, v179
	s_nop 0
	v_pk_mul_f32 v[58:59], v[58:59], v[172:173]
	v_pk_mul_f32 v[60:61], v[60:61], v[174:175]
	v_pk_mul_f32 v[50:51], v[50:51], v[176:177]
	v_pk_mul_f32 v[52:53], v[52:53], v[178:179]
	v_pk_mul_f32 v[58:59], v[62:63], v[58:59]
	v_pk_mul_f32 v[60:61], v[64:65], v[60:61]
	v_pk_mul_f32 v[50:51], v[54:55], v[50:51]
	v_pk_mul_f32 v[52:53], v[56:57], v[52:53]
	v_cvt_pk_bf16_f32 v58, v58, v59
	v_cvt_pk_bf16_f32 v59, v60, v61
	v_cvt_pk_bf16_f32 v60, v50, v51
	v_cvt_pk_bf16_f32 v61, v52, v53
	global_store_dwordx4 v[154:155], v[58:61], off
	v_pk_mul_f32 v[42:43], v[42:43], v[244:245] op_sel:[0,1] op_sel_hi:[1,1]
	v_pk_mul_f32 v[44:45], v[44:45], v[244:245] op_sel:[0,1] op_sel_hi:[1,1]
	v_pk_mul_f32 v[38:39], v[38:39], v[244:245] op_sel:[0,1] op_sel_hi:[1,1]
	v_pk_mul_f32 v[40:41], v[40:41], v[244:245] op_sel:[0,1] op_sel_hi:[1,1]
	v_pk_mul_f32 v[46:47], v[46:47], v[244:245] op_sel:[0,1] op_sel_hi:[1,1]
	v_pk_mul_f32 v[48:49], v[48:49], v[244:245] op_sel:[0,1] op_sel_hi:[1,1]
	v_pk_mul_f32 v[34:35], v[34:35], v[244:245] op_sel:[0,1] op_sel_hi:[1,1]
	v_pk_mul_f32 v[36:37], v[36:37], v[244:245] op_sel:[0,1] op_sel_hi:[1,1]
	v_pk_mul_f32 v[172:173], v[42:43], v[160:161]
	v_pk_mul_f32 v[174:175], v[44:45], v[160:161]
	v_pk_mul_f32 v[176:177], v[38:39], v[160:161]
	v_pk_mul_f32 v[178:179], v[40:41], v[160:161]
	v_exp_f32_e32 v172, v172
	v_exp_f32_e32 v173, v173
	v_exp_f32_e32 v174, v174
	v_exp_f32_e32 v175, v175
	v_exp_f32_e32 v176, v176
	v_exp_f32_e32 v177, v177
	v_exp_f32_e32 v178, v178
	v_exp_f32_e32 v179, v179
	s_mov_b32 s22, 0xc6000
	v_lshl_add_u64 v[156:157], s[22:23], 0, v[152:153]
	v_pk_add_f32 v[172:173], v[172:173], v[158:159]
	v_pk_add_f32 v[174:175], v[174:175], v[158:159]
	v_pk_add_f32 v[176:177], v[176:177], v[158:159]
	v_pk_add_f32 v[178:179], v[178:179], v[158:159]
	v_rcp_f32_e32 v172, v172
	v_rcp_f32_e32 v173, v173
	v_rcp_f32_e32 v174, v174
	v_rcp_f32_e32 v175, v175
	v_rcp_f32_e32 v176, v176
	v_rcp_f32_e32 v177, v177
	v_rcp_f32_e32 v178, v178
	v_rcp_f32_e32 v179, v179
	s_nop 0
	v_pk_mul_f32 v[42:43], v[42:43], v[172:173]
	v_pk_mul_f32 v[44:45], v[44:45], v[174:175]
	v_pk_mul_f32 v[38:39], v[38:39], v[176:177]
	v_pk_mul_f32 v[40:41], v[40:41], v[178:179]
	v_pk_mul_f32 v[42:43], v[46:47], v[42:43]
	v_pk_mul_f32 v[44:45], v[48:49], v[44:45]
	v_pk_mul_f32 v[38:39], v[34:35], v[38:39]
	v_pk_mul_f32 v[40:41], v[36:37], v[40:41]
	v_cvt_pk_bf16_f32 v42, v42, v43
	v_cvt_pk_bf16_f32 v43, v44, v45
	v_cvt_pk_bf16_f32 v44, v38, v39
	v_cvt_pk_bf16_f32 v45, v40, v41
	global_store_dwordx4 v[156:157], v[42:45], off
	v_pk_mul_f32 v[26:27], v[26:27], v[246:247] op_sel_hi:[1,0]
	v_pk_mul_f32 v[28:29], v[28:29], v[246:247] op_sel_hi:[1,0]
	v_pk_mul_f32 v[18:19], v[18:19], v[246:247] op_sel_hi:[1,0]
	v_pk_mul_f32 v[20:21], v[20:21], v[246:247] op_sel_hi:[1,0]
	v_pk_mul_f32 v[30:31], v[30:31], v[246:247] op_sel_hi:[1,0]
	v_pk_mul_f32 v[32:33], v[32:33], v[246:247] op_sel_hi:[1,0]
	v_pk_mul_f32 v[22:23], v[22:23], v[246:247] op_sel_hi:[1,0]
	v_pk_mul_f32 v[24:25], v[24:25], v[246:247] op_sel_hi:[1,0]
	v_pk_mul_f32 v[172:173], v[26:27], v[160:161]
	v_pk_mul_f32 v[174:175], v[28:29], v[160:161]
	v_pk_mul_f32 v[176:177], v[18:19], v[160:161]
	v_pk_mul_f32 v[178:179], v[20:21], v[160:161]
	v_exp_f32_e32 v172, v172
	v_exp_f32_e32 v173, v173
	v_exp_f32_e32 v174, v174
	v_exp_f32_e32 v175, v175
	v_exp_f32_e32 v176, v176
	v_exp_f32_e32 v177, v177
	v_exp_f32_e32 v178, v178
	v_exp_f32_e32 v179, v179
	s_mov_b32 s22, 0xdc000
	v_lshl_add_u64 v[154:155], s[22:23], 0, v[152:153]
	v_pk_add_f32 v[172:173], v[172:173], v[158:159]
	v_pk_add_f32 v[174:175], v[174:175], v[158:159]
	v_pk_add_f32 v[176:177], v[176:177], v[158:159]
	v_pk_add_f32 v[178:179], v[178:179], v[158:159]
	v_rcp_f32_e32 v172, v172
	v_rcp_f32_e32 v173, v173
	v_rcp_f32_e32 v174, v174
	v_rcp_f32_e32 v175, v175
	v_rcp_f32_e32 v176, v176
	v_rcp_f32_e32 v177, v177
	v_rcp_f32_e32 v178, v178
	v_rcp_f32_e32 v179, v179
	s_nop 0
	v_pk_mul_f32 v[26:27], v[26:27], v[172:173]
	v_pk_mul_f32 v[28:29], v[28:29], v[174:175]
	v_pk_mul_f32 v[18:19], v[18:19], v[176:177]
	v_pk_mul_f32 v[20:21], v[20:21], v[178:179]
	v_pk_mul_f32 v[26:27], v[30:31], v[26:27]
	v_pk_mul_f32 v[28:29], v[32:33], v[28:29]
	v_pk_mul_f32 v[18:19], v[22:23], v[18:19]
	v_pk_mul_f32 v[20:21], v[24:25], v[20:21]
	v_cvt_pk_bf16_f32 v26, v26, v27
	v_cvt_pk_bf16_f32 v27, v28, v29
	v_cvt_pk_bf16_f32 v28, v18, v19
	v_cvt_pk_bf16_f32 v29, v20, v21
	global_store_dwordx4 v[154:155], v[26:29], off
	v_pk_mul_f32 v[10:11], v[10:11], v[246:247] op_sel:[0,1] op_sel_hi:[1,1]
	v_pk_mul_f32 v[12:13], v[12:13], v[246:247] op_sel:[0,1] op_sel_hi:[1,1]
	v_pk_mul_f32 v[6:7], v[6:7], v[246:247] op_sel:[0,1] op_sel_hi:[1,1]
	v_pk_mul_f32 v[8:9], v[8:9], v[246:247] op_sel:[0,1] op_sel_hi:[1,1]
	v_pk_mul_f32 v[14:15], v[14:15], v[246:247] op_sel:[0,1] op_sel_hi:[1,1]
	v_pk_mul_f32 v[16:17], v[16:17], v[246:247] op_sel:[0,1] op_sel_hi:[1,1]
	v_pk_mul_f32 v[2:3], v[2:3], v[246:247] op_sel:[0,1] op_sel_hi:[1,1]
	v_pk_mul_f32 v[4:5], v[4:5], v[246:247] op_sel:[0,1] op_sel_hi:[1,1]
	v_pk_mul_f32 v[172:173], v[10:11], v[160:161]
	v_pk_mul_f32 v[174:175], v[12:13], v[160:161]
	v_pk_mul_f32 v[176:177], v[6:7], v[160:161]
	v_pk_mul_f32 v[178:179], v[8:9], v[160:161]
	v_exp_f32_e32 v172, v172
	v_exp_f32_e32 v173, v173
	v_exp_f32_e32 v174, v174
	v_exp_f32_e32 v175, v175
	v_exp_f32_e32 v176, v176
	v_exp_f32_e32 v177, v177
	v_exp_f32_e32 v178, v178
	v_exp_f32_e32 v179, v179
	s_mov_b32 s22, 0xf2000
	v_lshl_add_u64 v[156:157], s[22:23], 0, v[152:153]
	v_pk_add_f32 v[172:173], v[172:173], v[158:159]
	v_pk_add_f32 v[174:175], v[174:175], v[158:159]
	v_pk_add_f32 v[176:177], v[176:177], v[158:159]
	v_pk_add_f32 v[178:179], v[178:179], v[158:159]
	v_rcp_f32_e32 v172, v172
	v_rcp_f32_e32 v173, v173
	v_rcp_f32_e32 v174, v174
	v_rcp_f32_e32 v175, v175
	v_rcp_f32_e32 v176, v176
	v_rcp_f32_e32 v177, v177
	v_rcp_f32_e32 v178, v178
	v_rcp_f32_e32 v179, v179
	s_nop 0
	v_pk_mul_f32 v[10:11], v[10:11], v[172:173]
	v_pk_mul_f32 v[12:13], v[12:13], v[174:175]
	v_pk_mul_f32 v[6:7], v[6:7], v[176:177]
	v_pk_mul_f32 v[8:9], v[8:9], v[178:179]
	v_pk_mul_f32 v[10:11], v[14:15], v[10:11]
	v_pk_mul_f32 v[12:13], v[16:17], v[12:13]
	v_pk_mul_f32 v[6:7], v[2:3], v[6:7]
	v_pk_mul_f32 v[8:9], v[4:5], v[8:9]
	v_cvt_pk_bf16_f32 v10, v10, v11
	v_cvt_pk_bf16_f32 v11, v12, v13
	v_cvt_pk_bf16_f32 v12, v6, v7
	v_cvt_pk_bf16_f32 v13, v8, v9
	global_store_dwordx4 v[156:157], v[10:13], off
	s_mov_b64 s[22:23], -1
	s_and_b64 vcc, exec, s[2:3]
	s_cbranch_vccnz .LBB0_2793
	s_andn2_b64 vcc, exec, s[10:11]
	s_cbranch_vccnz .LBB0_2792
	s_barrier
	s_branch .LBB0_2792
